# loop-edge rotation in the seven 8-phase GEMM K-loops (SALU pointer/counter updates moved in front of the closing barrier); on top of v52
# speedup vs baseline: 1.0180x; 1.0001x over previous
.LBB0_299:
	ds_read_b128 v[156:159], v151
	ds_read_b128 v[160:163], v151 offset:1024
	ds_read_b128 v[164:167], v151 offset:2048
	ds_read_b128 v[168:171], v151 offset:3072
	ds_read_b128 v[172:175], v152
	ds_read_b128 v[176:179], v152 offset:1024
	ds_read_b128 v[180:183], v152 offset:2048
	ds_read_b128 v[184:187], v152 offset:3072
	s_add_u32 s24, s22, 0xfffc0080
	s_addc_u32 s25, s23, -1
	s_cmp_eq_u32 s52, 12
	s_cselect_b32 s27, s15, s25
	s_cselect_b32 s26, s48, s24
	s_cselect_b32 s25, s13, s51
	s_cselect_b32 s24, s49, s50
	v_lshl_add_u64 v[148:149], s[22:23], 0, v[138:139]
	s_add_i32 m0, s21, 0xc000
	ds_read_b128 v[192:195], v153
	ds_read_b128 v[196:199], v153 offset:1024
	ds_read_b128 v[200:203], v153 offset:2048
	ds_read_b128 v[204:207], v153 offset:3072
	ds_read_b128 v[208:211], v153 offset:4096
	ds_read_b128 v[212:215], v153 offset:5120
	ds_read_b128 v[216:219], v153 offset:6144
	ds_read_b128 v[224:227], v153 offset:7168
	global_load_lds_dwordx4 v[148:149], off
	v_lshl_add_u64 v[148:149], s[22:23], 0, v[140:141]
	s_add_i32 m0, s21, 0xe000
	s_nop 0
	global_load_lds_dwordx4 v[148:149], off
	s_waitcnt vmcnt(8)
	s_waitcnt lgkmcnt(0)
	s_barrier
	s_setprio 1
	s_waitcnt lgkmcnt(0)
	v_mfma_f32_16x16x32_bf16 v[126:129], v[156:159], v[192:195], v[126:129]
	v_mfma_f32_16x16x32_bf16 v[122:125], v[164:167], v[192:195], v[122:125]
	v_mfma_f32_16x16x32_bf16 v[114:117], v[156:159], v[200:203], v[114:117]
	v_mfma_f32_16x16x32_bf16 v[106:109], v[164:167], v[200:203], v[106:109]
	v_mfma_f32_16x16x32_bf16 v[98:101], v[156:159], v[208:211], v[98:101]
	v_mfma_f32_16x16x32_bf16 v[90:93], v[164:167], v[208:211], v[90:93]
	v_mfma_f32_16x16x32_bf16 v[82:85], v[156:159], v[216:219], v[82:85]
	v_mfma_f32_16x16x32_bf16 v[74:77], v[164:167], v[216:219], v[74:77]
	v_mfma_f32_16x16x32_bf16 v[126:129], v[160:163], v[196:199], v[126:129]
	v_mfma_f32_16x16x32_bf16 v[122:125], v[168:171], v[196:199], v[122:125]
	v_mfma_f32_16x16x32_bf16 v[114:117], v[160:163], v[204:207], v[114:117]
	v_mfma_f32_16x16x32_bf16 v[106:109], v[168:171], v[204:207], v[106:109]
	v_mfma_f32_16x16x32_bf16 v[98:101], v[160:163], v[212:215], v[98:101]
	v_mfma_f32_16x16x32_bf16 v[90:93], v[168:171], v[212:215], v[90:93]
	v_mfma_f32_16x16x32_bf16 v[82:85], v[160:163], v[224:227], v[82:85]
	v_mfma_f32_16x16x32_bf16 v[74:77], v[168:171], v[224:227], v[74:77]
	s_setprio 0
	s_setprio 1
	v_mfma_f32_16x16x32_bf16 v[118:121], v[172:175], v[192:195], v[118:121]
	v_mfma_f32_16x16x32_bf16 v[110:113], v[180:183], v[192:195], v[110:113]
	v_mfma_f32_16x16x32_bf16 v[102:105], v[172:175], v[200:203], v[102:105]
	v_mfma_f32_16x16x32_bf16 v[94:97], v[180:183], v[200:203], v[94:97]
	v_mfma_f32_16x16x32_bf16 v[86:89], v[172:175], v[208:211], v[86:89]
	v_mfma_f32_16x16x32_bf16 v[78:81], v[180:183], v[208:211], v[78:81]
	v_mfma_f32_16x16x32_bf16 v[70:73], v[172:175], v[216:219], v[70:73]
	v_mfma_f32_16x16x32_bf16 v[66:69], v[180:183], v[216:219], v[66:69]
	v_mfma_f32_16x16x32_bf16 v[118:121], v[176:179], v[196:199], v[118:121]
	v_mfma_f32_16x16x32_bf16 v[110:113], v[184:187], v[196:199], v[110:113]
	v_mfma_f32_16x16x32_bf16 v[102:105], v[176:179], v[204:207], v[102:105]
	v_mfma_f32_16x16x32_bf16 v[94:97], v[184:187], v[204:207], v[94:97]
	v_mfma_f32_16x16x32_bf16 v[86:89], v[176:179], v[212:215], v[86:89]
	v_mfma_f32_16x16x32_bf16 v[78:81], v[184:187], v[212:215], v[78:81]
	v_mfma_f32_16x16x32_bf16 v[70:73], v[176:179], v[224:227], v[70:73]
	v_mfma_f32_16x16x32_bf16 v[66:69], v[184:187], v[224:227], v[66:69]
	s_setprio 0
	s_barrier
	s_add_i32 s53, s44, s34
	v_lshl_add_u64 v[148:149], s[24:25], 0, v[134:135]
	s_mov_b32 m0, s53
	ds_read_b128 v[192:195], v153 offset:16384
	ds_read_b128 v[196:199], v153 offset:17408
	ds_read_b128 v[200:203], v153 offset:18432
	ds_read_b128 v[204:207], v153 offset:19456
	ds_read_b128 v[208:211], v153 offset:20480
	ds_read_b128 v[212:215], v153 offset:21504
	ds_read_b128 v[216:219], v153 offset:22528
	ds_read_b128 v[224:227], v153 offset:23552
	global_load_lds_dwordx4 v[148:149], off
	s_add_i32 m0, s53, 0x2000
	s_add_u32 s54, s24, 0x40000
	v_lshl_add_u64 v[188:189], s[24:25], 0, v[130:131]
	s_addc_u32 s55, s25, 0
	s_add_i32 s53, s45, s34
	global_load_lds_dwordx4 v[188:189], off
	v_lshl_add_u64 v[190:191], s[54:55], 0, v[134:135]
	s_mov_b32 m0, s53
	v_lshl_add_u64 v[220:221], s[26:27], 0, v[132:133]
	global_load_lds_dwordx4 v[190:191], off
	v_lshl_add_u64 v[190:191], s[54:55], 0, v[130:131]
	s_add_i32 m0, s53, 0x2000
	s_nop 0
	global_load_lds_dwordx4 v[190:191], off
	v_lshl_add_u64 v[190:191], s[26:27], 0, v[136:137]
	s_mov_b32 m0, s21
	s_nop 0
	global_load_lds_dwordx4 v[190:191], off
	s_mov_b32 m0, s37
	s_nop 0
	global_load_lds_dwordx4 v[220:221], off
	s_waitcnt vmcnt(8)
	s_waitcnt lgkmcnt(0)
	s_barrier
	s_setprio 1
	s_waitcnt lgkmcnt(0)
	v_mfma_f32_16x16x32_bf16 v[62:65], v[156:159], v[192:195], v[62:65]
	v_mfma_f32_16x16x32_bf16 v[58:61], v[164:167], v[192:195], v[58:61]
	v_mfma_f32_16x16x32_bf16 v[50:53], v[156:159], v[200:203], v[50:53]
	v_mfma_f32_16x16x32_bf16 v[42:45], v[164:167], v[200:203], v[42:45]
	v_mfma_f32_16x16x32_bf16 v[34:37], v[156:159], v[208:211], v[34:37]
	v_mfma_f32_16x16x32_bf16 v[26:29], v[164:167], v[208:211], v[26:29]
	v_mfma_f32_16x16x32_bf16 v[18:21], v[156:159], v[216:219], v[18:21]
	v_mfma_f32_16x16x32_bf16 v[10:13], v[164:167], v[216:219], v[10:13]
	v_mfma_f32_16x16x32_bf16 v[62:65], v[160:163], v[196:199], v[62:65]
	v_mfma_f32_16x16x32_bf16 v[58:61], v[168:171], v[196:199], v[58:61]
	v_mfma_f32_16x16x32_bf16 v[50:53], v[160:163], v[204:207], v[50:53]
	v_mfma_f32_16x16x32_bf16 v[42:45], v[168:171], v[204:207], v[42:45]
	v_mfma_f32_16x16x32_bf16 v[34:37], v[160:163], v[212:215], v[34:37]
	v_mfma_f32_16x16x32_bf16 v[26:29], v[168:171], v[212:215], v[26:29]
	v_mfma_f32_16x16x32_bf16 v[18:21], v[160:163], v[224:227], v[18:21]
	v_mfma_f32_16x16x32_bf16 v[10:13], v[168:171], v[224:227], v[10:13]
	s_setprio 0
	s_setprio 1
	v_mfma_f32_16x16x32_bf16 v[54:57], v[172:175], v[192:195], v[54:57]
	v_mfma_f32_16x16x32_bf16 v[46:49], v[180:183], v[192:195], v[46:49]
	v_mfma_f32_16x16x32_bf16 v[38:41], v[172:175], v[200:203], v[38:41]
	v_mfma_f32_16x16x32_bf16 v[30:33], v[180:183], v[200:203], v[30:33]
	v_mfma_f32_16x16x32_bf16 v[22:25], v[172:175], v[208:211], v[22:25]
	v_mfma_f32_16x16x32_bf16 v[14:17], v[180:183], v[208:211], v[14:17]
	v_mfma_f32_16x16x32_bf16 v[6:9], v[172:175], v[216:219], v[6:9]
	v_mfma_f32_16x16x32_bf16 v[2:5], v[180:183], v[216:219], v[2:5]
	v_mfma_f32_16x16x32_bf16 v[54:57], v[176:179], v[196:199], v[54:57]
	v_mfma_f32_16x16x32_bf16 v[46:49], v[184:187], v[196:199], v[46:49]
	v_mfma_f32_16x16x32_bf16 v[38:41], v[176:179], v[204:207], v[38:41]
	v_mfma_f32_16x16x32_bf16 v[30:33], v[184:187], v[204:207], v[30:33]
	v_mfma_f32_16x16x32_bf16 v[22:25], v[176:179], v[212:215], v[22:25]
	v_mfma_f32_16x16x32_bf16 v[14:17], v[184:187], v[212:215], v[14:17]
	v_mfma_f32_16x16x32_bf16 v[6:9], v[176:179], v[224:227], v[6:9]
	v_mfma_f32_16x16x32_bf16 v[2:5], v[184:187], v[224:227], v[2:5]
	s_setprio 0
	s_barrier
	s_add_i32 s53, 0, 0x18000
	v_add_u32_e32 v146, s53, v147
	s_add_i32 s54, 0, 0x1c000
	ds_read_b128 v[156:159], v146
	ds_read_b128 v[160:163], v146 offset:1024
	ds_read_b128 v[164:167], v146 offset:2048
	ds_read_b128 v[168:171], v146 offset:3072
	v_add_u32_e32 v146, s54, v147
	ds_read_b128 v[172:175], v146
	ds_read_b128 v[176:179], v146 offset:1024
	ds_read_b128 v[180:183], v146 offset:2048
	ds_read_b128 v[184:187], v146 offset:3072
	s_add_u32 s26, s26, 0x40000
	s_addc_u32 s27, s27, 0
	s_mov_b32 m0, s38
	v_lshl_add_u64 v[228:229], s[26:27], 0, v[136:137]
	ds_read_b128 v[192:195], v153 offset:32768
	ds_read_b128 v[196:199], v153 offset:33792
	ds_read_b128 v[200:203], v153 offset:34816
	ds_read_b128 v[204:207], v153 offset:35840
	ds_read_b128 v[208:211], v153 offset:36864
	ds_read_b128 v[212:215], v153 offset:37888
	ds_read_b128 v[216:219], v153 offset:38912
	ds_read_b128 v[224:227], v153 offset:39936
	global_load_lds_dwordx4 v[228:229], off
	v_lshl_add_u64 v[228:229], s[26:27], 0, v[132:133]
	s_mov_b32 m0, s39
	s_nop 0
	global_load_lds_dwordx4 v[228:229], off
	s_waitcnt vmcnt(8)
	s_waitcnt lgkmcnt(0)
	s_barrier
	s_setprio 1
	s_waitcnt lgkmcnt(0)
	v_mfma_f32_16x16x32_bf16 v[126:129], v[156:159], v[192:195], v[126:129]
	v_mfma_f32_16x16x32_bf16 v[122:125], v[164:167], v[192:195], v[122:125]
	v_mfma_f32_16x16x32_bf16 v[114:117], v[156:159], v[200:203], v[114:117]
	v_mfma_f32_16x16x32_bf16 v[106:109], v[164:167], v[200:203], v[106:109]
	v_mfma_f32_16x16x32_bf16 v[98:101], v[156:159], v[208:211], v[98:101]
	v_mfma_f32_16x16x32_bf16 v[90:93], v[164:167], v[208:211], v[90:93]
	v_mfma_f32_16x16x32_bf16 v[82:85], v[156:159], v[216:219], v[82:85]
	v_mfma_f32_16x16x32_bf16 v[74:77], v[164:167], v[216:219], v[74:77]
	v_mfma_f32_16x16x32_bf16 v[126:129], v[160:163], v[196:199], v[126:129]
	v_mfma_f32_16x16x32_bf16 v[122:125], v[168:171], v[196:199], v[122:125]
	v_mfma_f32_16x16x32_bf16 v[114:117], v[160:163], v[204:207], v[114:117]
	v_mfma_f32_16x16x32_bf16 v[106:109], v[168:171], v[204:207], v[106:109]
	v_mfma_f32_16x16x32_bf16 v[98:101], v[160:163], v[212:215], v[98:101]
	v_mfma_f32_16x16x32_bf16 v[90:93], v[168:171], v[212:215], v[90:93]
	v_mfma_f32_16x16x32_bf16 v[82:85], v[160:163], v[224:227], v[82:85]
	v_mfma_f32_16x16x32_bf16 v[74:77], v[168:171], v[224:227], v[74:77]
	s_setprio 0
	s_setprio 1
	v_mfma_f32_16x16x32_bf16 v[118:121], v[172:175], v[192:195], v[118:121]
	v_mfma_f32_16x16x32_bf16 v[110:113], v[180:183], v[192:195], v[110:113]
	v_mfma_f32_16x16x32_bf16 v[102:105], v[172:175], v[200:203], v[102:105]
	v_mfma_f32_16x16x32_bf16 v[94:97], v[180:183], v[200:203], v[94:97]
	v_mfma_f32_16x16x32_bf16 v[86:89], v[172:175], v[208:211], v[86:89]
	v_mfma_f32_16x16x32_bf16 v[78:81], v[180:183], v[208:211], v[78:81]
	v_mfma_f32_16x16x32_bf16 v[70:73], v[172:175], v[216:219], v[70:73]
	v_mfma_f32_16x16x32_bf16 v[66:69], v[180:183], v[216:219], v[66:69]
	v_mfma_f32_16x16x32_bf16 v[118:121], v[176:179], v[196:199], v[118:121]
	v_mfma_f32_16x16x32_bf16 v[110:113], v[184:187], v[196:199], v[110:113]
	v_mfma_f32_16x16x32_bf16 v[102:105], v[176:179], v[204:207], v[102:105]
	v_mfma_f32_16x16x32_bf16 v[94:97], v[184:187], v[204:207], v[94:97]
	v_mfma_f32_16x16x32_bf16 v[86:89], v[176:179], v[212:215], v[86:89]
	v_mfma_f32_16x16x32_bf16 v[78:81], v[184:187], v[212:215], v[78:81]
	v_mfma_f32_16x16x32_bf16 v[70:73], v[176:179], v[224:227], v[70:73]
	v_mfma_f32_16x16x32_bf16 v[66:69], v[184:187], v[224:227], v[66:69]
	s_setprio 0
	s_barrier
	s_add_i32 s26, s53, s34
	v_lshl_add_u64 v[148:149], v[148:149], 0, s[8:9]
	s_mov_b32 m0, s26
	ds_read_b128 v[192:195], v153 offset:49152
	ds_read_b128 v[196:199], v153 offset:50176
	ds_read_b128 v[200:203], v153 offset:51200
	ds_read_b128 v[204:207], v153 offset:52224
	ds_read_b128 v[208:211], v153 offset:53248
	ds_read_b128 v[212:215], v153 offset:54272
	ds_read_b128 v[216:219], v153 offset:55296
	ds_read_b128 v[224:227], v153 offset:56320
	global_load_lds_dwordx4 v[148:149], off
	s_add_i32 m0, s26, 0x2000
	s_add_u32 s24, s24, 0x40080
	v_lshl_add_u64 v[148:149], v[188:189], 0, s[8:9]
	s_addc_u32 s25, s25, 0
	s_add_i32 s26, s54, s34
	global_load_lds_dwordx4 v[148:149], off
	v_lshl_add_u64 v[148:149], s[24:25], 0, v[134:135]
	s_mov_b32 m0, s26
	s_nop 0
	global_load_lds_dwordx4 v[148:149], off
	v_lshl_add_u64 v[148:149], s[24:25], 0, v[130:131]
	s_add_i32 m0, s26, 0x2000
	s_nop 0
	global_load_lds_dwordx4 v[148:149], off
	v_lshl_add_u64 v[148:149], v[190:191], 0, s[8:9]
	s_mov_b32 m0, s41
	s_nop 0
	global_load_lds_dwordx4 v[148:149], off
	v_lshl_add_u64 v[148:149], v[220:221], 0, s[8:9]
	s_mov_b32 m0, s42
	s_nop 0
	global_load_lds_dwordx4 v[148:149], off
	s_waitcnt vmcnt(8)
	s_waitcnt lgkmcnt(0)
	s_barrier
	s_setprio 1
	s_waitcnt lgkmcnt(0)
	v_mfma_f32_16x16x32_bf16 v[62:65], v[156:159], v[192:195], v[62:65]
	v_mfma_f32_16x16x32_bf16 v[58:61], v[164:167], v[192:195], v[58:61]
	v_mfma_f32_16x16x32_bf16 v[50:53], v[156:159], v[200:203], v[50:53]
	v_mfma_f32_16x16x32_bf16 v[42:45], v[164:167], v[200:203], v[42:45]
	v_mfma_f32_16x16x32_bf16 v[34:37], v[156:159], v[208:211], v[34:37]
	v_mfma_f32_16x16x32_bf16 v[26:29], v[164:167], v[208:211], v[26:29]
	v_mfma_f32_16x16x32_bf16 v[18:21], v[156:159], v[216:219], v[18:21]
	v_mfma_f32_16x16x32_bf16 v[10:13], v[164:167], v[216:219], v[10:13]
	v_mfma_f32_16x16x32_bf16 v[62:65], v[160:163], v[196:199], v[62:65]
	v_mfma_f32_16x16x32_bf16 v[58:61], v[168:171], v[196:199], v[58:61]
	v_mfma_f32_16x16x32_bf16 v[50:53], v[160:163], v[204:207], v[50:53]
	v_mfma_f32_16x16x32_bf16 v[42:45], v[168:171], v[204:207], v[42:45]
	v_mfma_f32_16x16x32_bf16 v[34:37], v[160:163], v[212:215], v[34:37]
	v_mfma_f32_16x16x32_bf16 v[26:29], v[168:171], v[212:215], v[26:29]
	v_mfma_f32_16x16x32_bf16 v[18:21], v[160:163], v[224:227], v[18:21]
	v_mfma_f32_16x16x32_bf16 v[10:13], v[168:171], v[224:227], v[10:13]
	s_setprio 0
	s_setprio 1
	v_mfma_f32_16x16x32_bf16 v[54:57], v[172:175], v[192:195], v[54:57]
	v_mfma_f32_16x16x32_bf16 v[46:49], v[180:183], v[192:195], v[46:49]
	v_mfma_f32_16x16x32_bf16 v[38:41], v[172:175], v[200:203], v[38:41]
	v_mfma_f32_16x16x32_bf16 v[30:33], v[180:183], v[200:203], v[30:33]
	v_mfma_f32_16x16x32_bf16 v[22:25], v[172:175], v[208:211], v[22:25]
	v_mfma_f32_16x16x32_bf16 v[14:17], v[180:183], v[208:211], v[14:17]
	v_mfma_f32_16x16x32_bf16 v[6:9], v[172:175], v[216:219], v[6:9]
	v_mfma_f32_16x16x32_bf16 v[2:5], v[180:183], v[216:219], v[2:5]
	v_mfma_f32_16x16x32_bf16 v[54:57], v[176:179], v[196:199], v[54:57]
	v_mfma_f32_16x16x32_bf16 v[46:49], v[184:187], v[196:199], v[46:49]
	v_mfma_f32_16x16x32_bf16 v[38:41], v[176:179], v[204:207], v[38:41]
	v_mfma_f32_16x16x32_bf16 v[30:33], v[184:187], v[204:207], v[30:33]
	v_mfma_f32_16x16x32_bf16 v[22:25], v[176:179], v[212:215], v[22:25]
	v_mfma_f32_16x16x32_bf16 v[14:17], v[184:187], v[212:215], v[14:17]
	v_mfma_f32_16x16x32_bf16 v[6:9], v[176:179], v[224:227], v[6:9]
	v_mfma_f32_16x16x32_bf16 v[2:5], v[184:187], v[224:227], v[2:5]
	s_setprio 0
	s_add_i32 s52, s52, 2
	s_add_u32 s22, s22, 0x100
	s_addc_u32 s23, s23, 0
	s_add_u32 s50, s50, 0x100
	s_addc_u32 s51, s51, 0
	s_cmp_gt_u32 s52, 13
	s_barrier
	s_cbranch_scc0 .LBB0_299
	s_and_b64 vcc, exec, s[10:11]
	s_cbranch_vccz .LBB0_302
	s_barrier

.LBB0_836:
	ds_read_b128 v[146:149], v154
	ds_read_b128 v[160:163], v154 offset:1024
	ds_read_b128 v[164:167], v154 offset:2048
	ds_read_b128 v[168:171], v154 offset:3072
	ds_read_b128 v[172:175], v155
	ds_read_b128 v[176:179], v155 offset:1024
	ds_read_b128 v[180:183], v155 offset:2048
	ds_read_b128 v[184:187], v155 offset:3072
	s_add_u32 s24, s22, 0xfffc0080
	s_addc_u32 s25, s23, -1
	s_cmp_eq_u32 s46, 12
	s_cselect_b32 s27, s15, s25
	s_cselect_b32 s26, s42, s24
	s_cselect_b32 s25, s13, s45
	s_cselect_b32 s24, s43, s44
	v_lshl_add_u64 v[150:151], s[22:23], 0, v[138:139]
	s_add_i32 m0, s21, 0xc000
	ds_read_b128 v[194:197], v156
	ds_read_b128 v[198:201], v156 offset:1024
	ds_read_b128 v[202:205], v156 offset:2048
	ds_read_b128 v[210:213], v156 offset:3072
	ds_read_b128 v[214:217], v156 offset:4096
	ds_read_b128 v[218:221], v156 offset:5120
	ds_read_b128 v[230:233], v156 offset:6144
	ds_read_b128 v[234:237], v156 offset:7168
	global_load_lds_dwordx4 v[150:151], off
	v_lshl_add_u64 v[150:151], s[22:23], 0, v[140:141]
	s_add_i32 m0, s21, 0xe000
	s_nop 0
	global_load_lds_dwordx4 v[150:151], off
	s_waitcnt vmcnt(8)
	s_waitcnt lgkmcnt(0)
	s_barrier
	s_setprio 1
	s_waitcnt lgkmcnt(0)
	v_mfma_f32_16x16x32_bf16 v[126:129], v[146:149], v[194:197], v[126:129]
	v_mfma_f32_16x16x32_bf16 v[122:125], v[164:167], v[194:197], v[122:125]
	v_mfma_f32_16x16x32_bf16 v[118:121], v[146:149], v[202:205], v[118:121]
	v_mfma_f32_16x16x32_bf16 v[114:117], v[164:167], v[202:205], v[114:117]
	v_mfma_f32_16x16x32_bf16 v[94:97], v[146:149], v[214:217], v[94:97]
	v_mfma_f32_16x16x32_bf16 v[90:93], v[164:167], v[214:217], v[90:93]
	v_mfma_f32_16x16x32_bf16 v[86:89], v[146:149], v[230:233], v[86:89]
	v_mfma_f32_16x16x32_bf16 v[82:85], v[164:167], v[230:233], v[82:85]
	v_mfma_f32_16x16x32_bf16 v[126:129], v[160:163], v[198:201], v[126:129]
	v_mfma_f32_16x16x32_bf16 v[122:125], v[168:171], v[198:201], v[122:125]
	v_mfma_f32_16x16x32_bf16 v[118:121], v[160:163], v[210:213], v[118:121]
	v_mfma_f32_16x16x32_bf16 v[114:117], v[168:171], v[210:213], v[114:117]
	v_mfma_f32_16x16x32_bf16 v[94:97], v[160:163], v[218:221], v[94:97]
	v_mfma_f32_16x16x32_bf16 v[90:93], v[168:171], v[218:221], v[90:93]
	v_mfma_f32_16x16x32_bf16 v[86:89], v[160:163], v[234:237], v[86:89]
	v_mfma_f32_16x16x32_bf16 v[82:85], v[168:171], v[234:237], v[82:85]
	s_setprio 0
	s_setprio 1
	v_mfma_f32_16x16x32_bf16 v[110:113], v[172:175], v[194:197], v[110:113]
	v_mfma_f32_16x16x32_bf16 v[106:109], v[180:183], v[194:197], v[106:109]
	v_mfma_f32_16x16x32_bf16 v[102:105], v[172:175], v[202:205], v[102:105]
	v_mfma_f32_16x16x32_bf16 v[98:101], v[180:183], v[202:205], v[98:101]
	v_mfma_f32_16x16x32_bf16 v[78:81], v[172:175], v[214:217], v[78:81]
	v_mfma_f32_16x16x32_bf16 v[74:77], v[180:183], v[214:217], v[74:77]
	v_mfma_f32_16x16x32_bf16 v[70:73], v[172:175], v[230:233], v[70:73]
	v_mfma_f32_16x16x32_bf16 v[66:69], v[180:183], v[230:233], v[66:69]
	v_mfma_f32_16x16x32_bf16 v[110:113], v[176:179], v[198:201], v[110:113]
	v_mfma_f32_16x16x32_bf16 v[106:109], v[184:187], v[198:201], v[106:109]
	v_mfma_f32_16x16x32_bf16 v[102:105], v[176:179], v[210:213], v[102:105]
	v_mfma_f32_16x16x32_bf16 v[98:101], v[184:187], v[210:213], v[98:101]
	v_mfma_f32_16x16x32_bf16 v[78:81], v[176:179], v[218:221], v[78:81]
	v_mfma_f32_16x16x32_bf16 v[74:77], v[184:187], v[218:221], v[74:77]
	v_mfma_f32_16x16x32_bf16 v[70:73], v[176:179], v[234:237], v[70:73]
	v_mfma_f32_16x16x32_bf16 v[66:69], v[184:187], v[234:237], v[66:69]
	s_setprio 0
	s_barrier
	s_add_i32 s47, s39, s29
	v_lshl_add_u64 v[150:151], s[24:25], 0, v[132:133]
	s_mov_b32 m0, s47
	ds_read_b128 v[194:197], v156 offset:16384
	ds_read_b128 v[198:201], v156 offset:17408
	ds_read_b128 v[202:205], v156 offset:18432
	ds_read_b128 v[210:213], v156 offset:19456
	ds_read_b128 v[214:217], v156 offset:20480
	ds_read_b128 v[218:221], v156 offset:21504
	ds_read_b128 v[230:233], v156 offset:22528
	ds_read_b128 v[234:237], v156 offset:23552
	global_load_lds_dwordx4 v[150:151], off
	s_add_i32 m0, s47, 0x2000
	s_add_u32 s48, s24, 0x40000
	v_lshl_add_u64 v[188:189], s[24:25], 0, v[136:137]
	s_addc_u32 s49, s25, 0
	s_add_i32 s47, s40, s29
	global_load_lds_dwordx4 v[188:189], off
	v_lshl_add_u64 v[190:191], s[48:49], 0, v[132:133]
	s_mov_b32 m0, s47
	v_lshl_add_u64 v[206:207], s[26:27], 0, v[134:135]
	global_load_lds_dwordx4 v[190:191], off
	v_lshl_add_u64 v[190:191], s[48:49], 0, v[136:137]
	s_add_i32 m0, s47, 0x2000
	s_nop 0
	global_load_lds_dwordx4 v[190:191], off
	v_lshl_add_u64 v[190:191], s[26:27], 0, v[130:131]
	s_mov_b32 m0, s21
	s_nop 0
	global_load_lds_dwordx4 v[190:191], off
	s_mov_b32 m0, s30
	s_nop 0
	global_load_lds_dwordx4 v[206:207], off
	s_waitcnt vmcnt(8)
	s_waitcnt lgkmcnt(0)
	s_barrier
	s_setprio 1
	s_waitcnt lgkmcnt(0)
	v_mfma_f32_16x16x32_bf16 v[62:65], v[146:149], v[194:197], v[62:65]
	v_mfma_f32_16x16x32_bf16 v[58:61], v[164:167], v[194:197], v[58:61]
	v_mfma_f32_16x16x32_bf16 v[54:57], v[146:149], v[202:205], v[54:57]
	v_mfma_f32_16x16x32_bf16 v[50:53], v[164:167], v[202:205], v[50:53]
	v_mfma_f32_16x16x32_bf16 v[30:33], v[146:149], v[214:217], v[30:33]
	v_mfma_f32_16x16x32_bf16 v[26:29], v[164:167], v[214:217], v[26:29]
	v_mfma_f32_16x16x32_bf16 v[22:25], v[146:149], v[230:233], v[22:25]
	v_mfma_f32_16x16x32_bf16 v[18:21], v[164:167], v[230:233], v[18:21]
	v_mfma_f32_16x16x32_bf16 v[62:65], v[160:163], v[198:201], v[62:65]
	v_mfma_f32_16x16x32_bf16 v[58:61], v[168:171], v[198:201], v[58:61]
	v_mfma_f32_16x16x32_bf16 v[54:57], v[160:163], v[210:213], v[54:57]
	v_mfma_f32_16x16x32_bf16 v[50:53], v[168:171], v[210:213], v[50:53]
	v_mfma_f32_16x16x32_bf16 v[30:33], v[160:163], v[218:221], v[30:33]
	v_mfma_f32_16x16x32_bf16 v[26:29], v[168:171], v[218:221], v[26:29]
	v_mfma_f32_16x16x32_bf16 v[22:25], v[160:163], v[234:237], v[22:25]
	v_mfma_f32_16x16x32_bf16 v[18:21], v[168:171], v[234:237], v[18:21]
	s_setprio 0
	s_setprio 1
	v_mfma_f32_16x16x32_bf16 v[46:49], v[172:175], v[194:197], v[46:49]
	v_mfma_f32_16x16x32_bf16 v[42:45], v[180:183], v[194:197], v[42:45]
	v_mfma_f32_16x16x32_bf16 v[38:41], v[172:175], v[202:205], v[38:41]
	v_mfma_f32_16x16x32_bf16 v[34:37], v[180:183], v[202:205], v[34:37]
	v_mfma_f32_16x16x32_bf16 v[14:17], v[172:175], v[214:217], v[14:17]
	v_mfma_f32_16x16x32_bf16 v[10:13], v[180:183], v[214:217], v[10:13]
	v_mfma_f32_16x16x32_bf16 v[6:9], v[172:175], v[230:233], v[6:9]
	v_mfma_f32_16x16x32_bf16 v[2:5], v[180:183], v[230:233], v[2:5]
	v_mfma_f32_16x16x32_bf16 v[46:49], v[176:179], v[198:201], v[46:49]
	v_mfma_f32_16x16x32_bf16 v[42:45], v[184:187], v[198:201], v[42:45]
	v_mfma_f32_16x16x32_bf16 v[38:41], v[176:179], v[210:213], v[38:41]
	v_mfma_f32_16x16x32_bf16 v[34:37], v[184:187], v[210:213], v[34:37]
	v_mfma_f32_16x16x32_bf16 v[14:17], v[176:179], v[218:221], v[14:17]
	v_mfma_f32_16x16x32_bf16 v[10:13], v[184:187], v[218:221], v[10:13]
	v_mfma_f32_16x16x32_bf16 v[6:9], v[176:179], v[234:237], v[6:9]
	v_mfma_f32_16x16x32_bf16 v[2:5], v[184:187], v[234:237], v[2:5]
	s_setprio 0
	s_barrier
	s_add_i32 s47, 0, 0x18000
	v_add_u32_e32 v157, s47, v152
	s_add_i32 s48, 0, 0x1c000
	ds_read_b128 v[146:149], v157
	ds_read_b128 v[160:163], v157 offset:1024
	ds_read_b128 v[164:167], v157 offset:2048
	ds_read_b128 v[168:171], v157 offset:3072
	v_add_u32_e32 v157, s48, v152
	ds_read_b128 v[172:175], v157
	ds_read_b128 v[176:179], v157 offset:1024
	ds_read_b128 v[180:183], v157 offset:2048
	ds_read_b128 v[184:187], v157 offset:3072
	s_add_u32 s26, s26, 0x40000
	s_addc_u32 s27, s27, 0
	s_mov_b32 m0, s31
	v_lshl_add_u64 v[238:239], s[26:27], 0, v[130:131]
	ds_read_b128 v[194:197], v156 offset:32768
	ds_read_b128 v[198:201], v156 offset:33792
	ds_read_b128 v[202:205], v156 offset:34816
	ds_read_b128 v[210:213], v156 offset:35840
	ds_read_b128 v[214:217], v156 offset:36864
	ds_read_b128 v[218:221], v156 offset:37888
	ds_read_b128 v[230:233], v156 offset:38912
	ds_read_b128 v[234:237], v156 offset:39936
	global_load_lds_dwordx4 v[238:239], off
	v_lshl_add_u64 v[238:239], s[26:27], 0, v[134:135]
	s_mov_b32 m0, s34
	s_nop 0
	global_load_lds_dwordx4 v[238:239], off
	s_waitcnt vmcnt(8)
	s_waitcnt lgkmcnt(0)
	s_barrier
	s_setprio 1
	s_waitcnt lgkmcnt(0)
	v_mfma_f32_16x16x32_bf16 v[126:129], v[146:149], v[194:197], v[126:129]
	v_mfma_f32_16x16x32_bf16 v[122:125], v[164:167], v[194:197], v[122:125]
	v_mfma_f32_16x16x32_bf16 v[118:121], v[146:149], v[202:205], v[118:121]
	v_mfma_f32_16x16x32_bf16 v[114:117], v[164:167], v[202:205], v[114:117]
	v_mfma_f32_16x16x32_bf16 v[94:97], v[146:149], v[214:217], v[94:97]
	v_mfma_f32_16x16x32_bf16 v[90:93], v[164:167], v[214:217], v[90:93]
	v_mfma_f32_16x16x32_bf16 v[86:89], v[146:149], v[230:233], v[86:89]
	v_mfma_f32_16x16x32_bf16 v[82:85], v[164:167], v[230:233], v[82:85]
	v_mfma_f32_16x16x32_bf16 v[126:129], v[160:163], v[198:201], v[126:129]
	v_mfma_f32_16x16x32_bf16 v[122:125], v[168:171], v[198:201], v[122:125]
	v_mfma_f32_16x16x32_bf16 v[118:121], v[160:163], v[210:213], v[118:121]
	v_mfma_f32_16x16x32_bf16 v[114:117], v[168:171], v[210:213], v[114:117]
	v_mfma_f32_16x16x32_bf16 v[94:97], v[160:163], v[218:221], v[94:97]
	v_mfma_f32_16x16x32_bf16 v[90:93], v[168:171], v[218:221], v[90:93]
	v_mfma_f32_16x16x32_bf16 v[86:89], v[160:163], v[234:237], v[86:89]
	v_mfma_f32_16x16x32_bf16 v[82:85], v[168:171], v[234:237], v[82:85]
	s_setprio 0
	s_setprio 1
	v_mfma_f32_16x16x32_bf16 v[110:113], v[172:175], v[194:197], v[110:113]
	v_mfma_f32_16x16x32_bf16 v[106:109], v[180:183], v[194:197], v[106:109]
	v_mfma_f32_16x16x32_bf16 v[102:105], v[172:175], v[202:205], v[102:105]
	v_mfma_f32_16x16x32_bf16 v[98:101], v[180:183], v[202:205], v[98:101]
	v_mfma_f32_16x16x32_bf16 v[78:81], v[172:175], v[214:217], v[78:81]
	v_mfma_f32_16x16x32_bf16 v[74:77], v[180:183], v[214:217], v[74:77]
	v_mfma_f32_16x16x32_bf16 v[70:73], v[172:175], v[230:233], v[70:73]
	v_mfma_f32_16x16x32_bf16 v[66:69], v[180:183], v[230:233], v[66:69]
	v_mfma_f32_16x16x32_bf16 v[110:113], v[176:179], v[198:201], v[110:113]
	v_mfma_f32_16x16x32_bf16 v[106:109], v[184:187], v[198:201], v[106:109]
	v_mfma_f32_16x16x32_bf16 v[102:105], v[176:179], v[210:213], v[102:105]
	v_mfma_f32_16x16x32_bf16 v[98:101], v[184:187], v[210:213], v[98:101]
	v_mfma_f32_16x16x32_bf16 v[78:81], v[176:179], v[218:221], v[78:81]
	v_mfma_f32_16x16x32_bf16 v[74:77], v[184:187], v[218:221], v[74:77]
	v_mfma_f32_16x16x32_bf16 v[70:73], v[176:179], v[234:237], v[70:73]
	v_mfma_f32_16x16x32_bf16 v[66:69], v[184:187], v[234:237], v[66:69]
	s_setprio 0
	s_barrier
	s_add_i32 s26, s47, s29
	v_lshl_add_u64 v[150:151], v[150:151], 0, s[8:9]
	s_mov_b32 m0, s26
	ds_read_b128 v[194:197], v156 offset:49152
	ds_read_b128 v[198:201], v156 offset:50176
	ds_read_b128 v[202:205], v156 offset:51200
	ds_read_b128 v[210:213], v156 offset:52224
	ds_read_b128 v[214:217], v156 offset:53248
	ds_read_b128 v[218:221], v156 offset:54272
	ds_read_b128 v[230:233], v156 offset:55296
	ds_read_b128 v[234:237], v156 offset:56320
	global_load_lds_dwordx4 v[150:151], off
	s_add_i32 m0, s26, 0x2000
	s_add_u32 s24, s24, 0x40080
	v_lshl_add_u64 v[150:151], v[188:189], 0, s[8:9]
	s_addc_u32 s25, s25, 0
	s_add_i32 s26, s48, s29
	global_load_lds_dwordx4 v[150:151], off
	v_lshl_add_u64 v[150:151], s[24:25], 0, v[132:133]
	s_mov_b32 m0, s26
	s_nop 0
	global_load_lds_dwordx4 v[150:151], off
	v_lshl_add_u64 v[150:151], s[24:25], 0, v[136:137]
	s_add_i32 m0, s26, 0x2000
	s_nop 0
	global_load_lds_dwordx4 v[150:151], off
	v_lshl_add_u64 v[150:151], v[190:191], 0, s[8:9]
	s_mov_b32 m0, s36
	s_nop 0
	global_load_lds_dwordx4 v[150:151], off
	v_lshl_add_u64 v[150:151], v[206:207], 0, s[8:9]
	s_mov_b32 m0, s37
	s_nop 0
	global_load_lds_dwordx4 v[150:151], off
	s_waitcnt vmcnt(8)
	s_waitcnt lgkmcnt(0)
	s_barrier
	s_setprio 1
	s_waitcnt lgkmcnt(0)
	v_mfma_f32_16x16x32_bf16 v[62:65], v[146:149], v[194:197], v[62:65]
	v_mfma_f32_16x16x32_bf16 v[58:61], v[164:167], v[194:197], v[58:61]
	v_mfma_f32_16x16x32_bf16 v[54:57], v[146:149], v[202:205], v[54:57]
	v_mfma_f32_16x16x32_bf16 v[50:53], v[164:167], v[202:205], v[50:53]
	v_mfma_f32_16x16x32_bf16 v[30:33], v[146:149], v[214:217], v[30:33]
	v_mfma_f32_16x16x32_bf16 v[26:29], v[164:167], v[214:217], v[26:29]
	v_mfma_f32_16x16x32_bf16 v[22:25], v[146:149], v[230:233], v[22:25]
	v_mfma_f32_16x16x32_bf16 v[18:21], v[164:167], v[230:233], v[18:21]
	v_mfma_f32_16x16x32_bf16 v[62:65], v[160:163], v[198:201], v[62:65]
	v_mfma_f32_16x16x32_bf16 v[58:61], v[168:171], v[198:201], v[58:61]
	v_mfma_f32_16x16x32_bf16 v[54:57], v[160:163], v[210:213], v[54:57]
	v_mfma_f32_16x16x32_bf16 v[50:53], v[168:171], v[210:213], v[50:53]
	v_mfma_f32_16x16x32_bf16 v[30:33], v[160:163], v[218:221], v[30:33]
	v_mfma_f32_16x16x32_bf16 v[26:29], v[168:171], v[218:221], v[26:29]
	v_mfma_f32_16x16x32_bf16 v[22:25], v[160:163], v[234:237], v[22:25]
	v_mfma_f32_16x16x32_bf16 v[18:21], v[168:171], v[234:237], v[18:21]
	s_setprio 0
	s_setprio 1
	v_mfma_f32_16x16x32_bf16 v[46:49], v[172:175], v[194:197], v[46:49]
	v_mfma_f32_16x16x32_bf16 v[42:45], v[180:183], v[194:197], v[42:45]
	v_mfma_f32_16x16x32_bf16 v[38:41], v[172:175], v[202:205], v[38:41]
	v_mfma_f32_16x16x32_bf16 v[34:37], v[180:183], v[202:205], v[34:37]
	v_mfma_f32_16x16x32_bf16 v[14:17], v[172:175], v[214:217], v[14:17]
	v_mfma_f32_16x16x32_bf16 v[10:13], v[180:183], v[214:217], v[10:13]
	v_mfma_f32_16x16x32_bf16 v[6:9], v[172:175], v[230:233], v[6:9]
	v_mfma_f32_16x16x32_bf16 v[2:5], v[180:183], v[230:233], v[2:5]
	v_mfma_f32_16x16x32_bf16 v[46:49], v[176:179], v[198:201], v[46:49]
	v_mfma_f32_16x16x32_bf16 v[42:45], v[184:187], v[198:201], v[42:45]
	v_mfma_f32_16x16x32_bf16 v[38:41], v[176:179], v[210:213], v[38:41]
	v_mfma_f32_16x16x32_bf16 v[34:37], v[184:187], v[210:213], v[34:37]
	v_mfma_f32_16x16x32_bf16 v[14:17], v[176:179], v[218:221], v[14:17]
	v_mfma_f32_16x16x32_bf16 v[10:13], v[184:187], v[218:221], v[10:13]
	v_mfma_f32_16x16x32_bf16 v[6:9], v[176:179], v[234:237], v[6:9]
	v_mfma_f32_16x16x32_bf16 v[2:5], v[184:187], v[234:237], v[2:5]
	s_setprio 0
	s_add_i32 s46, s46, 2
	s_add_u32 s22, s22, 0x100
	s_addc_u32 s23, s23, 0
	s_add_u32 s44, s44, 0x100
	s_addc_u32 s45, s45, 0
	s_cmp_gt_u32 s46, 13
	s_barrier
	s_cbranch_scc0 .LBB0_836
	s_and_b64 vcc, exec, s[10:11]
	s_cbranch_vccz .LBB0_839
	s_barrier

.LBB0_1027:
	ds_read_b128 v[170:173], v167
	ds_read_b128 v[174:177], v167 offset:1024
	ds_read_b128 v[178:181], v167 offset:2048
	ds_read_b128 v[182:185], v167 offset:3072
	ds_read_b128 v[186:189], v168
	ds_read_b128 v[196:199], v168 offset:1024
	ds_read_b128 v[200:203], v168 offset:2048
	ds_read_b128 v[204:207], v168 offset:3072
	s_add_u32 s0, s20, 0x80
	s_addc_u32 s1, s21, 0
	s_cmp_eq_u32 s60, 12
	s_cselect_b32 s23, s83, s1
	s_cselect_b32 s22, s82, s0
	s_cselect_b32 s31, s17, s59
	s_cselect_b32 s30, s16, s58
	s_cselect_b32 s61, s57, s56
	ds_read_b128 v[210:213], v169 offset:1024
	ds_read_b128 v[214:217], v169 offset:2048
	ds_read_b128 v[218:221], v169 offset:3072
	ds_read_b128 v[230:233], v169 offset:4096
	ds_read_b128 v[234:237], v169
	ds_read2_b32 v[140:141], v138 offset0:2 offset1:3
	ds_read_b128 v[238:241], v169 offset:5120
	ds_read_b128 v[242:245], v169 offset:6144
	ds_read_b128 v[246:249], v169 offset:7168
	s_add_i32 m0, s37, 0xc000
	s_waitcnt lgkmcnt(0)
	global_load_lds_dwordx4 v140, s[20:21]
	s_add_i32 m0, s37, 0xe000
	s_nop 0
	global_load_lds_dwordx4 v141, s[20:21]
	s_waitcnt vmcnt(8)
	s_waitcnt lgkmcnt(0)
	s_barrier
	s_setprio 1
	v_mfma_f32_16x16x32_bf16 v[126:129], v[170:173], v[234:237], v[126:129]
	v_mfma_f32_16x16x32_bf16 v[122:125], v[178:181], v[234:237], v[122:125]
	v_mfma_f32_16x16x32_bf16 v[110:113], v[170:173], v[214:217], v[110:113]
	v_mfma_f32_16x16x32_bf16 v[106:109], v[178:181], v[214:217], v[106:109]
	v_mfma_f32_16x16x32_bf16 v[94:97], v[170:173], v[230:233], v[94:97]
	v_mfma_f32_16x16x32_bf16 v[82:85], v[178:181], v[230:233], v[82:85]
	v_mfma_f32_16x16x32_bf16 v[62:65], v[170:173], v[242:245], v[62:65]
	v_mfma_f32_16x16x32_bf16 v[46:49], v[178:181], v[242:245], v[46:49]
	v_mfma_f32_16x16x32_bf16 v[126:129], v[174:177], v[210:213], v[126:129]
	v_mfma_f32_16x16x32_bf16 v[122:125], v[182:185], v[210:213], v[122:125]
	v_mfma_f32_16x16x32_bf16 v[110:113], v[174:177], v[218:221], v[110:113]
	v_mfma_f32_16x16x32_bf16 v[106:109], v[182:185], v[218:221], v[106:109]
	v_mfma_f32_16x16x32_bf16 v[94:97], v[174:177], v[238:241], v[94:97]
	v_mfma_f32_16x16x32_bf16 v[82:85], v[182:185], v[238:241], v[82:85]
	v_mfma_f32_16x16x32_bf16 v[62:65], v[174:177], v[246:249], v[62:65]
	v_mfma_f32_16x16x32_bf16 v[46:49], v[182:185], v[246:249], v[46:49]
	s_setprio 0
	s_setprio 1
	v_mfma_f32_16x16x32_bf16 v[118:121], v[186:189], v[234:237], v[118:121]
	v_mfma_f32_16x16x32_bf16 v[114:117], v[200:203], v[234:237], v[114:117]
	v_mfma_f32_16x16x32_bf16 v[102:105], v[186:189], v[214:217], v[102:105]
	v_mfma_f32_16x16x32_bf16 v[98:101], v[200:203], v[214:217], v[98:101]
	v_mfma_f32_16x16x32_bf16 v[74:77], v[186:189], v[230:233], v[74:77]
	v_mfma_f32_16x16x32_bf16 v[66:69], v[200:203], v[230:233], v[66:69]
	v_mfma_f32_16x16x32_bf16 v[38:41], v[186:189], v[242:245], v[38:41]
	v_mfma_f32_16x16x32_bf16 v[34:37], v[200:203], v[242:245], v[34:37]
	v_mfma_f32_16x16x32_bf16 v[118:121], v[196:199], v[210:213], v[118:121]
	v_mfma_f32_16x16x32_bf16 v[114:117], v[204:207], v[210:213], v[114:117]
	v_mfma_f32_16x16x32_bf16 v[102:105], v[196:199], v[218:221], v[102:105]
	v_mfma_f32_16x16x32_bf16 v[98:101], v[204:207], v[218:221], v[98:101]
	v_mfma_f32_16x16x32_bf16 v[74:77], v[196:199], v[238:241], v[74:77]
	v_mfma_f32_16x16x32_bf16 v[66:69], v[204:207], v[238:241], v[66:69]
	v_mfma_f32_16x16x32_bf16 v[38:41], v[196:199], v[246:249], v[38:41]
	v_mfma_f32_16x16x32_bf16 v[34:37], v[204:207], v[246:249], v[34:37]
	s_setprio 0
	s_barrier
	s_add_i32 s0, s43, s36
	v_lshl_add_u64 v[140:141], s[30:31], 0, v[134:135]
	s_mov_b32 m0, s0
	ds_read_b128 v[210:213], v169 offset:16384
	ds_read_b128 v[214:217], v169 offset:17408
	ds_read_b128 v[218:221], v169 offset:18432
	ds_read_b128 v[230:233], v169 offset:19456
	ds_read_b128 v[234:237], v169 offset:20480
	ds_read_b128 v[238:241], v169 offset:21504
	ds_read_b128 v[242:245], v169 offset:22528
	ds_read_b128 v[246:249], v169 offset:23552
	global_load_lds_dwordx4 v[140:141], off
	s_add_i32 m0, s0, 0x2000
	s_add_u32 s0, s30, 0x40000
	v_lshl_add_u64 v[190:191], s[30:31], 0, v[132:133]
	s_addc_u32 s1, s31, 0
	s_add_i32 s62, s44, s36
	global_load_lds_dwordx4 v[190:191], off
	v_lshl_add_u64 v[208:209], s[0:1], 0, v[134:135]
	s_mov_b32 m0, s62
	v_lshl_add_u32 v136, s61, 2, v153
	global_load_lds_dwordx4 v[208:209], off
	v_lshl_add_u64 v[208:209], s[0:1], 0, v[132:133]
	s_add_i32 m0, s62, 0x2000
	s_nop 0
	global_load_lds_dwordx4 v[208:209], off
	ds_read2_b32 v[208:209], v136 offset1:1
	s_mov_b32 m0, s37
	s_waitcnt lgkmcnt(0)
	global_load_lds_dwordx4 v208, s[22:23]
	s_mov_b32 m0, s38
	s_nop 0
	global_load_lds_dwordx4 v209, s[22:23]
	s_waitcnt vmcnt(8)
	s_waitcnt lgkmcnt(0)
	s_barrier
	s_setprio 1
	v_mfma_f32_16x16x32_bf16 v[90:93], v[170:173], v[210:213], v[90:93]
	v_mfma_f32_16x16x32_bf16 v[78:81], v[178:181], v[210:213], v[78:81]
	v_mfma_f32_16x16x32_bf16 v[58:61], v[170:173], v[218:221], v[58:61]
	v_mfma_f32_16x16x32_bf16 v[50:53], v[178:181], v[218:221], v[50:53]
	v_mfma_f32_16x16x32_bf16 v[30:33], v[170:173], v[234:237], v[30:33]
	v_mfma_f32_16x16x32_bf16 v[22:25], v[178:181], v[234:237], v[22:25]
	v_mfma_f32_16x16x32_bf16 v[14:17], v[170:173], v[242:245], v[14:17]
	v_mfma_f32_16x16x32_bf16 v[6:9], v[178:181], v[242:245], v[6:9]
	v_mfma_f32_16x16x32_bf16 v[90:93], v[174:177], v[214:217], v[90:93]
	v_mfma_f32_16x16x32_bf16 v[78:81], v[182:185], v[214:217], v[78:81]
	v_mfma_f32_16x16x32_bf16 v[58:61], v[174:177], v[230:233], v[58:61]
	v_mfma_f32_16x16x32_bf16 v[50:53], v[182:185], v[230:233], v[50:53]
	v_mfma_f32_16x16x32_bf16 v[30:33], v[174:177], v[238:241], v[30:33]
	v_mfma_f32_16x16x32_bf16 v[22:25], v[182:185], v[238:241], v[22:25]
	v_mfma_f32_16x16x32_bf16 v[14:17], v[174:177], v[246:249], v[14:17]
	v_mfma_f32_16x16x32_bf16 v[6:9], v[182:185], v[246:249], v[6:9]
	s_setprio 0
	s_setprio 1
	v_mfma_f32_16x16x32_bf16 v[86:89], v[186:189], v[210:213], v[86:89]
	v_mfma_f32_16x16x32_bf16 v[70:73], v[200:203], v[210:213], v[70:73]
	v_mfma_f32_16x16x32_bf16 v[54:57], v[186:189], v[218:221], v[54:57]
	v_mfma_f32_16x16x32_bf16 v[42:45], v[200:203], v[218:221], v[42:45]
	v_mfma_f32_16x16x32_bf16 v[26:29], v[186:189], v[234:237], v[26:29]
	v_mfma_f32_16x16x32_bf16 v[18:21], v[200:203], v[234:237], v[18:21]
	v_mfma_f32_16x16x32_bf16 v[10:13], v[186:189], v[242:245], v[10:13]
	v_mfma_f32_16x16x32_bf16 v[2:5], v[200:203], v[242:245], v[2:5]
	v_mfma_f32_16x16x32_bf16 v[86:89], v[196:199], v[214:217], v[86:89]
	v_mfma_f32_16x16x32_bf16 v[70:73], v[204:207], v[214:217], v[70:73]
	v_mfma_f32_16x16x32_bf16 v[54:57], v[196:199], v[230:233], v[54:57]
	v_mfma_f32_16x16x32_bf16 v[42:45], v[204:207], v[230:233], v[42:45]
	v_mfma_f32_16x16x32_bf16 v[26:29], v[196:199], v[238:241], v[26:29]
	v_mfma_f32_16x16x32_bf16 v[18:21], v[204:207], v[238:241], v[18:21]
	v_mfma_f32_16x16x32_bf16 v[10:13], v[196:199], v[246:249], v[10:13]
	v_mfma_f32_16x16x32_bf16 v[2:5], v[204:207], v[246:249], v[2:5]
	s_setprio 0
	s_barrier
	s_add_i32 s0, 0, 0x18000
	v_add_u32_e32 v139, s0, v156
	s_add_i32 s61, 0, 0x1c000
	ds_read_b128 v[170:173], v139
	ds_read_b128 v[174:177], v139 offset:1024
	ds_read_b128 v[178:181], v139 offset:2048
	ds_read_b128 v[182:185], v139 offset:3072
	v_add_u32_e32 v139, s61, v156
	ds_read_b128 v[186:189], v139
	ds_read_b128 v[196:199], v139 offset:1024
	ds_read_b128 v[200:203], v139 offset:2048
	ds_read_b128 v[204:207], v139 offset:3072
	ds_read_b128 v[210:213], v169 offset:32768
	ds_read_b128 v[214:217], v169 offset:33792
	ds_read_b128 v[218:221], v169 offset:34816
	ds_read_b128 v[230:233], v169 offset:35840
	ds_read_b128 v[234:237], v169 offset:36864
	ds_read_b128 v[238:241], v169 offset:37888
	ds_read2_b32 v[208:209], v136 offset0:2 offset1:3
	ds_read_b128 v[242:245], v169 offset:38912
	ds_read_b128 v[246:249], v169 offset:39936
	s_mov_b32 m0, s39
	s_waitcnt lgkmcnt(0)
	global_load_lds_dwordx4 v208, s[22:23]
	s_mov_b32 m0, s40
	s_nop 0
	global_load_lds_dwordx4 v209, s[22:23]
	s_waitcnt vmcnt(8)
	s_waitcnt lgkmcnt(0)
	s_barrier
	s_setprio 1
	v_mfma_f32_16x16x32_bf16 v[126:129], v[170:173], v[210:213], v[126:129]
	v_mfma_f32_16x16x32_bf16 v[122:125], v[178:181], v[210:213], v[122:125]
	v_mfma_f32_16x16x32_bf16 v[110:113], v[170:173], v[218:221], v[110:113]
	v_mfma_f32_16x16x32_bf16 v[106:109], v[178:181], v[218:221], v[106:109]
	v_mfma_f32_16x16x32_bf16 v[94:97], v[170:173], v[234:237], v[94:97]
	v_mfma_f32_16x16x32_bf16 v[82:85], v[178:181], v[234:237], v[82:85]
	v_mfma_f32_16x16x32_bf16 v[62:65], v[170:173], v[242:245], v[62:65]
	v_mfma_f32_16x16x32_bf16 v[46:49], v[178:181], v[242:245], v[46:49]
	v_mfma_f32_16x16x32_bf16 v[126:129], v[174:177], v[214:217], v[126:129]
	v_mfma_f32_16x16x32_bf16 v[122:125], v[182:185], v[214:217], v[122:125]
	v_mfma_f32_16x16x32_bf16 v[110:113], v[174:177], v[230:233], v[110:113]
	v_mfma_f32_16x16x32_bf16 v[106:109], v[182:185], v[230:233], v[106:109]
	v_mfma_f32_16x16x32_bf16 v[94:97], v[174:177], v[238:241], v[94:97]
	v_mfma_f32_16x16x32_bf16 v[82:85], v[182:185], v[238:241], v[82:85]
	v_mfma_f32_16x16x32_bf16 v[62:65], v[174:177], v[246:249], v[62:65]
	v_mfma_f32_16x16x32_bf16 v[46:49], v[182:185], v[246:249], v[46:49]
	s_setprio 0
	s_setprio 1
	v_mfma_f32_16x16x32_bf16 v[118:121], v[186:189], v[210:213], v[118:121]
	v_mfma_f32_16x16x32_bf16 v[114:117], v[200:203], v[210:213], v[114:117]
	v_mfma_f32_16x16x32_bf16 v[102:105], v[186:189], v[218:221], v[102:105]
	v_mfma_f32_16x16x32_bf16 v[98:101], v[200:203], v[218:221], v[98:101]
	v_mfma_f32_16x16x32_bf16 v[74:77], v[186:189], v[234:237], v[74:77]
	v_mfma_f32_16x16x32_bf16 v[66:69], v[200:203], v[234:237], v[66:69]
	v_mfma_f32_16x16x32_bf16 v[38:41], v[186:189], v[242:245], v[38:41]
	v_mfma_f32_16x16x32_bf16 v[34:37], v[200:203], v[242:245], v[34:37]
	v_mfma_f32_16x16x32_bf16 v[118:121], v[196:199], v[214:217], v[118:121]
	v_mfma_f32_16x16x32_bf16 v[114:117], v[204:207], v[214:217], v[114:117]
	v_mfma_f32_16x16x32_bf16 v[102:105], v[196:199], v[230:233], v[102:105]
	v_mfma_f32_16x16x32_bf16 v[98:101], v[204:207], v[230:233], v[98:101]
	v_mfma_f32_16x16x32_bf16 v[74:77], v[196:199], v[238:241], v[74:77]
	v_mfma_f32_16x16x32_bf16 v[66:69], v[204:207], v[238:241], v[66:69]
	v_mfma_f32_16x16x32_bf16 v[38:41], v[196:199], v[246:249], v[38:41]
	v_mfma_f32_16x16x32_bf16 v[34:37], v[204:207], v[246:249], v[34:37]
	s_setprio 0
	s_barrier
	s_add_i32 s0, s0, s36
	v_lshl_add_u64 v[140:141], v[140:141], 0, s[10:11]
	s_mov_b32 m0, s0
	ds_read_b128 v[210:213], v169 offset:49152
	ds_read_b128 v[214:217], v169 offset:50176
	ds_read_b128 v[218:221], v169 offset:51200
	ds_read_b128 v[230:233], v169 offset:52224
	ds_read_b128 v[234:237], v169 offset:53248
	ds_read_b128 v[238:241], v169 offset:54272
	ds_read_b128 v[242:245], v169 offset:55296
	ds_read_b128 v[246:249], v169 offset:56320
	global_load_lds_dwordx4 v[140:141], off
	s_add_i32 m0, s0, 0x2000
	s_add_u32 s0, s30, 0x40080
	v_lshl_add_u64 v[140:141], v[190:191], 0, s[10:11]
	s_addc_u32 s1, s31, 0
	s_add_i32 s30, s61, s36
	global_load_lds_dwordx4 v[140:141], off
	v_lshl_add_u64 v[140:141], s[0:1], 0, v[134:135]
	s_mov_b32 m0, s30
	s_nop 0
	global_load_lds_dwordx4 v[140:141], off
	v_lshl_add_u64 v[140:141], s[0:1], 0, v[132:133]
	s_add_i32 m0, s30, 0x2000
	s_nop 0
	global_load_lds_dwordx4 v[140:141], off
	ds_read2_b32 v[140:141], v136 offset1:1
	s_mov_b32 m0, s41
	s_waitcnt lgkmcnt(0)
	v_mov_b32_e32 v136, v140
	v_lshl_add_u64 v[190:191], s[22:23], 0, v[136:137]
	v_mov_b32_e32 v136, v141
	v_lshl_add_u64 v[190:191], v[190:191], 0, s[10:11]
	v_lshl_add_u64 v[140:141], s[22:23], 0, v[136:137]
	global_load_lds_dwordx4 v[190:191], off
	v_lshl_add_u64 v[140:141], v[140:141], 0, s[10:11]
	s_mov_b32 m0, s42
	s_nop 0
	global_load_lds_dwordx4 v[140:141], off
	s_waitcnt vmcnt(8)
	s_waitcnt lgkmcnt(0)
	s_barrier
	s_setprio 1
	v_mfma_f32_16x16x32_bf16 v[90:93], v[170:173], v[210:213], v[90:93]
	v_mfma_f32_16x16x32_bf16 v[78:81], v[178:181], v[210:213], v[78:81]
	v_mfma_f32_16x16x32_bf16 v[58:61], v[170:173], v[218:221], v[58:61]
	v_mfma_f32_16x16x32_bf16 v[50:53], v[178:181], v[218:221], v[50:53]
	v_mfma_f32_16x16x32_bf16 v[30:33], v[170:173], v[234:237], v[30:33]
	v_mfma_f32_16x16x32_bf16 v[22:25], v[178:181], v[234:237], v[22:25]
	v_mfma_f32_16x16x32_bf16 v[14:17], v[170:173], v[242:245], v[14:17]
	v_mfma_f32_16x16x32_bf16 v[6:9], v[178:181], v[242:245], v[6:9]
	v_mfma_f32_16x16x32_bf16 v[90:93], v[174:177], v[214:217], v[90:93]
	v_mfma_f32_16x16x32_bf16 v[78:81], v[182:185], v[214:217], v[78:81]
	v_mfma_f32_16x16x32_bf16 v[58:61], v[174:177], v[230:233], v[58:61]
	v_mfma_f32_16x16x32_bf16 v[50:53], v[182:185], v[230:233], v[50:53]
	v_mfma_f32_16x16x32_bf16 v[30:33], v[174:177], v[238:241], v[30:33]
	v_mfma_f32_16x16x32_bf16 v[22:25], v[182:185], v[238:241], v[22:25]
	v_mfma_f32_16x16x32_bf16 v[14:17], v[174:177], v[246:249], v[14:17]
	v_mfma_f32_16x16x32_bf16 v[6:9], v[182:185], v[246:249], v[6:9]
	s_setprio 0
	s_setprio 1
	v_mfma_f32_16x16x32_bf16 v[86:89], v[186:189], v[210:213], v[86:89]
	v_mfma_f32_16x16x32_bf16 v[70:73], v[200:203], v[210:213], v[70:73]
	v_mfma_f32_16x16x32_bf16 v[54:57], v[186:189], v[218:221], v[54:57]
	v_mfma_f32_16x16x32_bf16 v[42:45], v[200:203], v[218:221], v[42:45]
	v_mfma_f32_16x16x32_bf16 v[26:29], v[186:189], v[234:237], v[26:29]
	v_mfma_f32_16x16x32_bf16 v[18:21], v[200:203], v[234:237], v[18:21]
	v_mfma_f32_16x16x32_bf16 v[10:13], v[186:189], v[242:245], v[10:13]
	v_mfma_f32_16x16x32_bf16 v[2:5], v[200:203], v[242:245], v[2:5]
	v_mfma_f32_16x16x32_bf16 v[86:89], v[196:199], v[214:217], v[86:89]
	v_mfma_f32_16x16x32_bf16 v[70:73], v[204:207], v[214:217], v[70:73]
	v_mfma_f32_16x16x32_bf16 v[54:57], v[196:199], v[230:233], v[54:57]
	v_mfma_f32_16x16x32_bf16 v[42:45], v[204:207], v[230:233], v[42:45]
	v_mfma_f32_16x16x32_bf16 v[26:29], v[196:199], v[238:241], v[26:29]
	v_mfma_f32_16x16x32_bf16 v[18:21], v[204:207], v[238:241], v[18:21]
	v_mfma_f32_16x16x32_bf16 v[10:13], v[196:199], v[246:249], v[10:13]
	v_mfma_f32_16x16x32_bf16 v[2:5], v[204:207], v[246:249], v[2:5]
	s_setprio 0
	s_add_i32 s60, s60, 2
	s_add_u32 s20, s20, 0x100
	s_addc_u32 s21, s21, 0
	s_add_u32 s58, s58, 0x100
	s_addc_u32 s59, s59, 0
	s_cmp_gt_u32 s60, 13
	s_barrier
	s_cbranch_scc0 .LBB0_1027
	v_and_b32_e32 v208, 63, v0

.LBB0_1479:
	s_waitcnt vmcnt(0)
	ds_read_b128 v[66:69], v214
	ds_read_b128 v[70:73], v214 offset:1024
	ds_read_b128 v[74:77], v214 offset:2048
	ds_read_b128 v[78:81], v214 offset:3072
	ds_read_b128 v[170:173], v215
	ds_read_b128 v[174:177], v215 offset:1024
	ds_read_b128 v[178:181], v215 offset:2048
	ds_read_b128 v[182:185], v215 offset:3072
	s_add_u32 s36, s6, 0xfffc0080
	s_addc_u32 s37, s7, -1
	s_cmp_eq_u32 s66, 12
	s_cselect_b32 s39, s9, s37
	s_cselect_b32 s38, s21, s36
	s_cselect_b32 s37, s19, s65
	s_cselect_b32 s36, s35, s64
	v_lshl_add_u64 v[190:191], s[6:7], 0, v[162:163]
	s_add_i32 m0, s41, 0xc000
	ds_read_b128 v[186:189], v216
	ds_read_b128 v[196:199], v216 offset:1024
	ds_read_b128 v[200:203], v216 offset:2048
	ds_read_b128 v[204:207], v216 offset:3072
	ds_read_b128 v[218:221], v216 offset:4096
	ds_read_b128 v[230:233], v216 offset:5120
	ds_read_b128 v[234:237], v216 offset:6144
	ds_read_b128 v[238:241], v216 offset:7168
	global_load_lds_dwordx4 v[190:191], off
	v_lshl_add_u64 v[190:191], s[6:7], 0, v[164:165]
	s_add_i32 m0, s41, 0xe000
	s_nop 0
	global_load_lds_dwordx4 v[190:191], off
	s_waitcnt vmcnt(8)
	s_waitcnt lgkmcnt(0)
	s_barrier
	s_setprio 1
	s_waitcnt lgkmcnt(0)
	v_mfma_f32_16x16x32_bf16 v[142:145], v[66:69], v[186:189], v[142:145]
	v_mfma_f32_16x16x32_bf16 v[138:141], v[74:77], v[186:189], v[138:141]
	v_mfma_f32_16x16x32_bf16 v[126:129], v[66:69], v[200:203], v[126:129]
	v_mfma_f32_16x16x32_bf16 v[122:125], v[74:77], v[200:203], v[122:125]
	v_mfma_f32_16x16x32_bf16 v[110:113], v[66:69], v[218:221], v[110:113]
	v_mfma_f32_16x16x32_bf16 v[106:109], v[74:77], v[218:221], v[106:109]
	v_mfma_f32_16x16x32_bf16 v[94:97], v[66:69], v[234:237], v[94:97]
	v_mfma_f32_16x16x32_bf16 v[90:93], v[74:77], v[234:237], v[90:93]
	v_mfma_f32_16x16x32_bf16 v[142:145], v[70:73], v[196:199], v[142:145]
	v_mfma_f32_16x16x32_bf16 v[138:141], v[78:81], v[196:199], v[138:141]
	v_mfma_f32_16x16x32_bf16 v[126:129], v[70:73], v[204:207], v[126:129]
	v_mfma_f32_16x16x32_bf16 v[122:125], v[78:81], v[204:207], v[122:125]
	v_mfma_f32_16x16x32_bf16 v[110:113], v[70:73], v[230:233], v[110:113]
	v_mfma_f32_16x16x32_bf16 v[106:109], v[78:81], v[230:233], v[106:109]
	v_mfma_f32_16x16x32_bf16 v[94:97], v[70:73], v[238:241], v[94:97]
	v_mfma_f32_16x16x32_bf16 v[90:93], v[78:81], v[238:241], v[90:93]
	s_setprio 0
	s_setprio 1
	v_mfma_f32_16x16x32_bf16 v[134:137], v[170:173], v[186:189], v[134:137]
	v_mfma_f32_16x16x32_bf16 v[130:133], v[178:181], v[186:189], v[130:133]
	v_mfma_f32_16x16x32_bf16 v[118:121], v[170:173], v[200:203], v[118:121]
	v_mfma_f32_16x16x32_bf16 v[114:117], v[178:181], v[200:203], v[114:117]
	v_mfma_f32_16x16x32_bf16 v[102:105], v[170:173], v[218:221], v[102:105]
	v_mfma_f32_16x16x32_bf16 v[98:101], v[178:181], v[218:221], v[98:101]
	v_mfma_f32_16x16x32_bf16 v[86:89], v[170:173], v[234:237], v[86:89]
	v_mfma_f32_16x16x32_bf16 v[82:85], v[178:181], v[234:237], v[82:85]
	v_mfma_f32_16x16x32_bf16 v[134:137], v[174:177], v[196:199], v[134:137]
	v_mfma_f32_16x16x32_bf16 v[130:133], v[182:185], v[196:199], v[130:133]
	v_mfma_f32_16x16x32_bf16 v[118:121], v[174:177], v[204:207], v[118:121]
	v_mfma_f32_16x16x32_bf16 v[114:117], v[182:185], v[204:207], v[114:117]
	v_mfma_f32_16x16x32_bf16 v[102:105], v[174:177], v[230:233], v[102:105]
	v_mfma_f32_16x16x32_bf16 v[98:101], v[182:185], v[230:233], v[98:101]
	v_mfma_f32_16x16x32_bf16 v[86:89], v[174:177], v[238:241], v[86:89]
	v_mfma_f32_16x16x32_bf16 v[82:85], v[182:185], v[238:241], v[82:85]
	s_setprio 0
	s_barrier
	s_add_i32 s67, s52, s40
	v_lshl_add_u64 v[190:191], s[36:37], 0, v[148:149]
	s_mov_b32 m0, s67
	ds_read_b128 v[186:189], v216 offset:16384
	ds_read_b128 v[196:199], v216 offset:17408
	ds_read_b128 v[200:203], v216 offset:18432
	ds_read_b128 v[204:207], v216 offset:19456
	ds_read_b128 v[218:221], v216 offset:20480
	ds_read_b128 v[230:233], v216 offset:21504
	ds_read_b128 v[234:237], v216 offset:22528
	ds_read_b128 v[238:241], v216 offset:23552
	global_load_lds_dwordx4 v[190:191], off
	s_add_i32 m0, s67, 0x2000
	s_add_u32 s68, s36, 0x10000
	v_lshl_add_u64 v[242:243], s[36:37], 0, v[152:153]
	s_addc_u32 s69, s37, 0
	s_add_i32 s67, s53, s40
	global_load_lds_dwordx4 v[242:243], off
	v_lshl_add_u64 v[244:245], s[68:69], 0, v[148:149]
	s_mov_b32 m0, s67
	v_lshl_add_u64 v[246:247], s[38:39], 0, v[150:151]
	global_load_lds_dwordx4 v[244:245], off
	v_lshl_add_u64 v[244:245], s[68:69], 0, v[152:153]
	s_add_i32 m0, s67, 0x2000
	s_nop 0
	global_load_lds_dwordx4 v[244:245], off
	v_lshl_add_u64 v[244:245], s[38:39], 0, v[146:147]
	s_mov_b32 m0, s41
	s_nop 0
	global_load_lds_dwordx4 v[244:245], off
	s_mov_b32 m0, s42
	s_nop 0
	global_load_lds_dwordx4 v[246:247], off
	s_waitcnt vmcnt(8)
	s_waitcnt lgkmcnt(0)
	s_barrier
	s_setprio 1
	s_waitcnt lgkmcnt(0)
	v_mfma_f32_16x16x32_bf16 v[62:65], v[66:69], v[186:189], v[62:65]
	v_mfma_f32_16x16x32_bf16 v[58:61], v[74:77], v[186:189], v[58:61]
	v_mfma_f32_16x16x32_bf16 v[46:49], v[66:69], v[200:203], v[46:49]
	v_mfma_f32_16x16x32_bf16 v[42:45], v[74:77], v[200:203], v[42:45]
	v_mfma_f32_16x16x32_bf16 v[30:33], v[66:69], v[218:221], v[30:33]
	v_mfma_f32_16x16x32_bf16 v[26:29], v[74:77], v[218:221], v[26:29]
	v_mfma_f32_16x16x32_bf16 v[14:17], v[66:69], v[234:237], v[14:17]
	v_mfma_f32_16x16x32_bf16 v[10:13], v[74:77], v[234:237], v[10:13]
	v_mfma_f32_16x16x32_bf16 v[62:65], v[70:73], v[196:199], v[62:65]
	v_mfma_f32_16x16x32_bf16 v[58:61], v[78:81], v[196:199], v[58:61]
	v_mfma_f32_16x16x32_bf16 v[46:49], v[70:73], v[204:207], v[46:49]
	v_mfma_f32_16x16x32_bf16 v[42:45], v[78:81], v[204:207], v[42:45]
	v_mfma_f32_16x16x32_bf16 v[30:33], v[70:73], v[230:233], v[30:33]
	v_mfma_f32_16x16x32_bf16 v[26:29], v[78:81], v[230:233], v[26:29]
	v_mfma_f32_16x16x32_bf16 v[14:17], v[70:73], v[238:241], v[14:17]
	v_mfma_f32_16x16x32_bf16 v[10:13], v[78:81], v[238:241], v[10:13]
	s_setprio 0
	s_setprio 1
	v_mfma_f32_16x16x32_bf16 v[54:57], v[170:173], v[186:189], v[54:57]
	v_mfma_f32_16x16x32_bf16 v[50:53], v[178:181], v[186:189], v[50:53]
	v_mfma_f32_16x16x32_bf16 v[38:41], v[170:173], v[200:203], v[38:41]
	v_mfma_f32_16x16x32_bf16 v[34:37], v[178:181], v[200:203], v[34:37]
	v_mfma_f32_16x16x32_bf16 v[22:25], v[170:173], v[218:221], v[22:25]
	v_mfma_f32_16x16x32_bf16 v[18:21], v[178:181], v[218:221], v[18:21]
	v_mfma_f32_16x16x32_bf16 v[6:9], v[170:173], v[234:237], v[6:9]
	v_mfma_f32_16x16x32_bf16 v[2:5], v[178:181], v[234:237], v[2:5]
	v_mfma_f32_16x16x32_bf16 v[54:57], v[174:177], v[196:199], v[54:57]
	v_mfma_f32_16x16x32_bf16 v[50:53], v[182:185], v[196:199], v[50:53]
	v_mfma_f32_16x16x32_bf16 v[38:41], v[174:177], v[204:207], v[38:41]
	v_mfma_f32_16x16x32_bf16 v[34:37], v[182:185], v[204:207], v[34:37]
	v_mfma_f32_16x16x32_bf16 v[22:25], v[174:177], v[230:233], v[22:25]
	v_mfma_f32_16x16x32_bf16 v[18:21], v[182:185], v[230:233], v[18:21]
	v_mfma_f32_16x16x32_bf16 v[6:9], v[174:177], v[238:241], v[6:9]
	v_mfma_f32_16x16x32_bf16 v[2:5], v[182:185], v[238:241], v[2:5]
	s_setprio 0
	s_barrier
	s_add_i32 s67, 0, 0x18000
	s_add_i32 s68, 0, 0x1c000
	v_add_u32_e32 v78, s67, v212
	v_add_u32_e32 v156, s68, v212
	ds_read_b128 v[66:69], v78
	ds_read_b128 v[70:73], v78 offset:1024
	ds_read_b128 v[74:77], v78 offset:2048
	ds_read_b128 v[78:81], v78 offset:3072
	ds_read_b128 v[170:173], v156
	ds_read_b128 v[174:177], v156 offset:1024
	ds_read_b128 v[178:181], v156 offset:2048
	ds_read_b128 v[182:185], v156 offset:3072
	s_add_u32 s38, s38, 0x40000
	s_addc_u32 s39, s39, 0
	s_mov_b32 m0, s43
	v_lshl_add_u64 v[248:249], s[38:39], 0, v[146:147]
	ds_read_b128 v[186:189], v216 offset:32768
	ds_read_b128 v[196:199], v216 offset:33792
	ds_read_b128 v[200:203], v216 offset:34816
	ds_read_b128 v[204:207], v216 offset:35840
	ds_read_b128 v[218:221], v216 offset:36864
	ds_read_b128 v[230:233], v216 offset:37888
	ds_read_b128 v[234:237], v216 offset:38912
	ds_read_b128 v[238:241], v216 offset:39936
	global_load_lds_dwordx4 v[248:249], off
	v_lshl_add_u64 v[248:249], s[38:39], 0, v[150:151]
	s_mov_b32 m0, s44
	s_nop 0
	global_load_lds_dwordx4 v[248:249], off
	s_waitcnt vmcnt(8)
	s_waitcnt lgkmcnt(0)
	s_barrier
	s_setprio 1
	s_waitcnt lgkmcnt(0)
	v_mfma_f32_16x16x32_bf16 v[142:145], v[66:69], v[186:189], v[142:145]
	v_mfma_f32_16x16x32_bf16 v[138:141], v[74:77], v[186:189], v[138:141]
	v_mfma_f32_16x16x32_bf16 v[126:129], v[66:69], v[200:203], v[126:129]
	v_mfma_f32_16x16x32_bf16 v[122:125], v[74:77], v[200:203], v[122:125]
	v_mfma_f32_16x16x32_bf16 v[110:113], v[66:69], v[218:221], v[110:113]
	v_mfma_f32_16x16x32_bf16 v[106:109], v[74:77], v[218:221], v[106:109]
	v_mfma_f32_16x16x32_bf16 v[94:97], v[66:69], v[234:237], v[94:97]
	v_mfma_f32_16x16x32_bf16 v[90:93], v[74:77], v[234:237], v[90:93]
	v_mfma_f32_16x16x32_bf16 v[142:145], v[70:73], v[196:199], v[142:145]
	v_mfma_f32_16x16x32_bf16 v[138:141], v[78:81], v[196:199], v[138:141]
	v_mfma_f32_16x16x32_bf16 v[126:129], v[70:73], v[204:207], v[126:129]
	v_mfma_f32_16x16x32_bf16 v[122:125], v[78:81], v[204:207], v[122:125]
	v_mfma_f32_16x16x32_bf16 v[110:113], v[70:73], v[230:233], v[110:113]
	v_mfma_f32_16x16x32_bf16 v[106:109], v[78:81], v[230:233], v[106:109]
	v_mfma_f32_16x16x32_bf16 v[94:97], v[70:73], v[238:241], v[94:97]
	v_mfma_f32_16x16x32_bf16 v[90:93], v[78:81], v[238:241], v[90:93]
	s_setprio 0
	s_setprio 1
	v_mfma_f32_16x16x32_bf16 v[134:137], v[170:173], v[186:189], v[134:137]
	v_mfma_f32_16x16x32_bf16 v[130:133], v[178:181], v[186:189], v[130:133]
	v_mfma_f32_16x16x32_bf16 v[118:121], v[170:173], v[200:203], v[118:121]
	v_mfma_f32_16x16x32_bf16 v[114:117], v[178:181], v[200:203], v[114:117]
	v_mfma_f32_16x16x32_bf16 v[102:105], v[170:173], v[218:221], v[102:105]
	v_mfma_f32_16x16x32_bf16 v[98:101], v[178:181], v[218:221], v[98:101]
	v_mfma_f32_16x16x32_bf16 v[86:89], v[170:173], v[234:237], v[86:89]
	v_mfma_f32_16x16x32_bf16 v[82:85], v[178:181], v[234:237], v[82:85]
	v_mfma_f32_16x16x32_bf16 v[134:137], v[174:177], v[196:199], v[134:137]
	v_mfma_f32_16x16x32_bf16 v[130:133], v[182:185], v[196:199], v[130:133]
	v_mfma_f32_16x16x32_bf16 v[118:121], v[174:177], v[204:207], v[118:121]
	v_mfma_f32_16x16x32_bf16 v[114:117], v[182:185], v[204:207], v[114:117]
	v_mfma_f32_16x16x32_bf16 v[102:105], v[174:177], v[230:233], v[102:105]
	v_mfma_f32_16x16x32_bf16 v[98:101], v[182:185], v[230:233], v[98:101]
	v_mfma_f32_16x16x32_bf16 v[86:89], v[174:177], v[238:241], v[86:89]
	v_mfma_f32_16x16x32_bf16 v[82:85], v[182:185], v[238:241], v[82:85]
	s_setprio 0
	s_barrier
	s_add_i32 s38, s67, s40
	v_lshl_add_u64 v[190:191], v[190:191], 0, s[14:15]
	s_mov_b32 m0, s38
	ds_read_b128 v[186:189], v216 offset:49152
	ds_read_b128 v[196:199], v216 offset:50176
	ds_read_b128 v[200:203], v216 offset:51200
	ds_read_b128 v[204:207], v216 offset:52224
	ds_read_b128 v[218:221], v216 offset:53248
	ds_read_b128 v[230:233], v216 offset:54272
	ds_read_b128 v[234:237], v216 offset:55296
	ds_read_b128 v[238:241], v216 offset:56320
	global_load_lds_dwordx4 v[190:191], off
	s_add_i32 m0, s38, 0x2000
	s_add_u32 s36, s36, 0x10080
	v_lshl_add_u64 v[190:191], v[242:243], 0, s[14:15]
	s_addc_u32 s37, s37, 0
	s_add_i32 s38, s68, s40
	global_load_lds_dwordx4 v[190:191], off
	v_lshl_add_u64 v[190:191], s[36:37], 0, v[148:149]
	s_mov_b32 m0, s38
	s_nop 0
	global_load_lds_dwordx4 v[190:191], off
	v_lshl_add_u64 v[190:191], s[36:37], 0, v[152:153]
	s_add_i32 m0, s38, 0x2000
	s_nop 0
	global_load_lds_dwordx4 v[190:191], off
	v_lshl_add_u64 v[190:191], v[244:245], 0, s[14:15]
	s_mov_b32 m0, s48
	s_nop 0
	global_load_lds_dwordx4 v[190:191], off
	v_lshl_add_u64 v[190:191], v[246:247], 0, s[14:15]
	s_mov_b32 m0, s49
	s_nop 0
	global_load_lds_dwordx4 v[190:191], off
	s_waitcnt vmcnt(8)
	s_waitcnt lgkmcnt(0)
	s_barrier
	s_setprio 1
	s_waitcnt lgkmcnt(0)
	v_mfma_f32_16x16x32_bf16 v[62:65], v[66:69], v[186:189], v[62:65]
	v_mfma_f32_16x16x32_bf16 v[58:61], v[74:77], v[186:189], v[58:61]
	v_mfma_f32_16x16x32_bf16 v[46:49], v[66:69], v[200:203], v[46:49]
	v_mfma_f32_16x16x32_bf16 v[42:45], v[74:77], v[200:203], v[42:45]
	v_mfma_f32_16x16x32_bf16 v[30:33], v[66:69], v[218:221], v[30:33]
	v_mfma_f32_16x16x32_bf16 v[26:29], v[74:77], v[218:221], v[26:29]
	v_mfma_f32_16x16x32_bf16 v[14:17], v[66:69], v[234:237], v[14:17]
	v_mfma_f32_16x16x32_bf16 v[10:13], v[74:77], v[234:237], v[10:13]
	v_mfma_f32_16x16x32_bf16 v[62:65], v[70:73], v[196:199], v[62:65]
	v_mfma_f32_16x16x32_bf16 v[58:61], v[78:81], v[196:199], v[58:61]
	v_mfma_f32_16x16x32_bf16 v[46:49], v[70:73], v[204:207], v[46:49]
	v_mfma_f32_16x16x32_bf16 v[42:45], v[78:81], v[204:207], v[42:45]
	v_mfma_f32_16x16x32_bf16 v[30:33], v[70:73], v[230:233], v[30:33]
	v_mfma_f32_16x16x32_bf16 v[26:29], v[78:81], v[230:233], v[26:29]
	v_mfma_f32_16x16x32_bf16 v[14:17], v[70:73], v[238:241], v[14:17]
	v_mfma_f32_16x16x32_bf16 v[10:13], v[78:81], v[238:241], v[10:13]
	s_setprio 0
	s_setprio 1
	v_mfma_f32_16x16x32_bf16 v[54:57], v[170:173], v[186:189], v[54:57]
	v_mfma_f32_16x16x32_bf16 v[50:53], v[178:181], v[186:189], v[50:53]
	v_mfma_f32_16x16x32_bf16 v[38:41], v[170:173], v[200:203], v[38:41]
	v_mfma_f32_16x16x32_bf16 v[34:37], v[178:181], v[200:203], v[34:37]
	v_mfma_f32_16x16x32_bf16 v[22:25], v[170:173], v[218:221], v[22:25]
	v_mfma_f32_16x16x32_bf16 v[18:21], v[178:181], v[218:221], v[18:21]
	v_mfma_f32_16x16x32_bf16 v[6:9], v[170:173], v[234:237], v[6:9]
	v_mfma_f32_16x16x32_bf16 v[2:5], v[178:181], v[234:237], v[2:5]
	v_mfma_f32_16x16x32_bf16 v[54:57], v[174:177], v[196:199], v[54:57]
	v_mfma_f32_16x16x32_bf16 v[50:53], v[182:185], v[196:199], v[50:53]
	v_mfma_f32_16x16x32_bf16 v[38:41], v[174:177], v[204:207], v[38:41]
	v_mfma_f32_16x16x32_bf16 v[34:37], v[182:185], v[204:207], v[34:37]
	v_mfma_f32_16x16x32_bf16 v[22:25], v[174:177], v[230:233], v[22:25]
	v_mfma_f32_16x16x32_bf16 v[18:21], v[182:185], v[230:233], v[18:21]
	v_mfma_f32_16x16x32_bf16 v[6:9], v[174:177], v[238:241], v[6:9]
	v_mfma_f32_16x16x32_bf16 v[2:5], v[182:185], v[238:241], v[2:5]
	s_setprio 0
	s_add_i32 s66, s66, 2
	s_add_u32 s6, s6, 0x100
	s_addc_u32 s7, s7, 0
	s_add_u32 s64, s64, 0x100
	s_addc_u32 s65, s65, 0
	s_cmp_gt_u32 s66, 13
	s_barrier
	s_cbranch_scc0 .LBB0_1479
	s_and_b64 vcc, exec, s[16:17]
	s_cbranch_vccz .LBB0_1482
	s_barrier

.LBB0_1599:
	ds_read_b128 v[140:143], v1
	ds_read_b128 v[154:157], v1 offset:1024
	ds_read_b128 v[160:163], v1 offset:2048
	ds_read_b128 v[164:167], v1 offset:3072
	ds_read_b128 v[176:179], v159
	ds_read_b128 v[180:183], v159 offset:1024
	ds_read_b128 v[184:187], v159 offset:2048
	ds_read_b128 v[196:199], v159 offset:3072
	s_add_u32 s38, s36, 0xfffc0080
	s_addc_u32 s39, s37, -1
	s_cmp_eq_u32 s64, 12
	s_cselect_b32 s41, s21, s39
	s_cselect_b32 s40, s60, s38
	s_cselect_b32 s39, s19, s63
	s_cselect_b32 s38, s61, s62
	v_lshl_add_u64 v[144:145], s[36:37], 0, v[132:133]
	s_add_i32 m0, s35, 0xc000
	ds_read_b128 v[200:203], v173
	ds_read_b128 v[204:207], v173 offset:1024
	ds_read_b128 v[210:213], v173 offset:2048
	ds_read_b128 v[214:217], v173 offset:3072
	ds_read_b128 v[218:221], v173 offset:4096
	ds_read_b128 v[230:233], v173 offset:5120
	ds_read_b128 v[234:237], v173 offset:6144
	ds_read_b128 v[238:241], v173 offset:7168
	global_load_lds_dwordx4 v[144:145], off
	v_lshl_add_u64 v[144:145], s[36:37], 0, v[134:135]
	s_add_i32 m0, s35, 0xe000
	s_nop 0
	global_load_lds_dwordx4 v[144:145], off
	s_waitcnt vmcnt(8)
	s_waitcnt lgkmcnt(0)
	s_barrier
	s_setprio 1
	s_waitcnt lgkmcnt(0)
	v_mfma_f32_16x16x32_bf16 v[126:129], v[140:143], v[200:203], v[126:129]
	v_mfma_f32_16x16x32_bf16 v[122:125], v[160:163], v[200:203], v[122:125]
	v_mfma_f32_16x16x32_bf16 v[114:117], v[140:143], v[210:213], v[114:117]
	v_mfma_f32_16x16x32_bf16 v[106:109], v[160:163], v[210:213], v[106:109]
	v_mfma_f32_16x16x32_bf16 v[98:101], v[140:143], v[218:221], v[98:101]
	v_mfma_f32_16x16x32_bf16 v[90:93], v[160:163], v[218:221], v[90:93]
	v_mfma_f32_16x16x32_bf16 v[82:85], v[140:143], v[234:237], v[82:85]
	v_mfma_f32_16x16x32_bf16 v[74:77], v[160:163], v[234:237], v[74:77]
	v_mfma_f32_16x16x32_bf16 v[126:129], v[154:157], v[204:207], v[126:129]
	v_mfma_f32_16x16x32_bf16 v[122:125], v[164:167], v[204:207], v[122:125]
	v_mfma_f32_16x16x32_bf16 v[114:117], v[154:157], v[214:217], v[114:117]
	v_mfma_f32_16x16x32_bf16 v[106:109], v[164:167], v[214:217], v[106:109]
	v_mfma_f32_16x16x32_bf16 v[98:101], v[154:157], v[230:233], v[98:101]
	v_mfma_f32_16x16x32_bf16 v[90:93], v[164:167], v[230:233], v[90:93]
	v_mfma_f32_16x16x32_bf16 v[82:85], v[154:157], v[238:241], v[82:85]
	v_mfma_f32_16x16x32_bf16 v[74:77], v[164:167], v[238:241], v[74:77]
	s_setprio 0
	s_setprio 1
	v_mfma_f32_16x16x32_bf16 v[118:121], v[176:179], v[200:203], v[118:121]
	v_mfma_f32_16x16x32_bf16 v[110:113], v[184:187], v[200:203], v[110:113]
	v_mfma_f32_16x16x32_bf16 v[102:105], v[176:179], v[210:213], v[102:105]
	v_mfma_f32_16x16x32_bf16 v[94:97], v[184:187], v[210:213], v[94:97]
	v_mfma_f32_16x16x32_bf16 v[86:89], v[176:179], v[218:221], v[86:89]
	v_mfma_f32_16x16x32_bf16 v[78:81], v[184:187], v[218:221], v[78:81]
	v_mfma_f32_16x16x32_bf16 v[70:73], v[176:179], v[234:237], v[70:73]
	v_mfma_f32_16x16x32_bf16 v[66:69], v[184:187], v[234:237], v[66:69]
	v_mfma_f32_16x16x32_bf16 v[118:121], v[180:183], v[204:207], v[118:121]
	v_mfma_f32_16x16x32_bf16 v[110:113], v[196:199], v[204:207], v[110:113]
	v_mfma_f32_16x16x32_bf16 v[102:105], v[180:183], v[214:217], v[102:105]
	v_mfma_f32_16x16x32_bf16 v[94:97], v[196:199], v[214:217], v[94:97]
	v_mfma_f32_16x16x32_bf16 v[86:89], v[180:183], v[230:233], v[86:89]
	v_mfma_f32_16x16x32_bf16 v[78:81], v[196:199], v[230:233], v[78:81]
	v_mfma_f32_16x16x32_bf16 v[70:73], v[180:183], v[238:241], v[70:73]
	v_mfma_f32_16x16x32_bf16 v[66:69], v[196:199], v[238:241], v[66:69]
	s_setprio 0
	s_barrier
	s_add_i32 s65, s50, s42
	v_lshl_add_u64 v[144:145], s[38:39], 0, v[148:149]
	s_mov_b32 m0, s65
	ds_read_b128 v[200:203], v173 offset:16384
	ds_read_b128 v[204:207], v173 offset:17408
	ds_read_b128 v[210:213], v173 offset:18432
	ds_read_b128 v[214:217], v173 offset:19456
	ds_read_b128 v[218:221], v173 offset:20480
	ds_read_b128 v[230:233], v173 offset:21504
	ds_read_b128 v[234:237], v173 offset:22528
	ds_read_b128 v[238:241], v173 offset:23552
	global_load_lds_dwordx4 v[144:145], off
	s_add_i32 m0, s65, 0x2000
	s_add_u32 s66, s38, 0x10000
	v_lshl_add_u64 v[168:169], s[38:39], 0, v[152:153]
	s_addc_u32 s67, s39, 0
	s_add_i32 s65, s51, s42
	global_load_lds_dwordx4 v[168:169], off
	v_lshl_add_u64 v[188:189], s[66:67], 0, v[148:149]
	s_mov_b32 m0, s65
	v_lshl_add_u64 v[190:191], s[40:41], 0, v[150:151]
	global_load_lds_dwordx4 v[188:189], off
	v_lshl_add_u64 v[188:189], s[66:67], 0, v[152:153]
	s_add_i32 m0, s65, 0x2000
	s_nop 0
	global_load_lds_dwordx4 v[188:189], off
	v_lshl_add_u64 v[188:189], s[40:41], 0, v[146:147]
	s_mov_b32 m0, s35
	s_nop 0
	global_load_lds_dwordx4 v[188:189], off
	s_mov_b32 m0, s43
	s_nop 0
	global_load_lds_dwordx4 v[190:191], off
	s_waitcnt vmcnt(8)
	s_waitcnt lgkmcnt(0)
	s_barrier
	s_setprio 1
	s_waitcnt lgkmcnt(0)
	v_mfma_f32_16x16x32_bf16 v[62:65], v[140:143], v[200:203], v[62:65]
	v_mfma_f32_16x16x32_bf16 v[58:61], v[160:163], v[200:203], v[58:61]
	v_mfma_f32_16x16x32_bf16 v[50:53], v[140:143], v[210:213], v[50:53]
	v_mfma_f32_16x16x32_bf16 v[42:45], v[160:163], v[210:213], v[42:45]
	v_mfma_f32_16x16x32_bf16 v[34:37], v[140:143], v[218:221], v[34:37]
	v_mfma_f32_16x16x32_bf16 v[26:29], v[160:163], v[218:221], v[26:29]
	v_mfma_f32_16x16x32_bf16 v[18:21], v[140:143], v[234:237], v[18:21]
	v_mfma_f32_16x16x32_bf16 v[10:13], v[160:163], v[234:237], v[10:13]
	v_mfma_f32_16x16x32_bf16 v[62:65], v[154:157], v[204:207], v[62:65]
	v_mfma_f32_16x16x32_bf16 v[58:61], v[164:167], v[204:207], v[58:61]
	v_mfma_f32_16x16x32_bf16 v[50:53], v[154:157], v[214:217], v[50:53]
	v_mfma_f32_16x16x32_bf16 v[42:45], v[164:167], v[214:217], v[42:45]
	v_mfma_f32_16x16x32_bf16 v[34:37], v[154:157], v[230:233], v[34:37]
	v_mfma_f32_16x16x32_bf16 v[26:29], v[164:167], v[230:233], v[26:29]
	v_mfma_f32_16x16x32_bf16 v[18:21], v[154:157], v[238:241], v[18:21]
	v_mfma_f32_16x16x32_bf16 v[10:13], v[164:167], v[238:241], v[10:13]
	s_setprio 0
	s_setprio 1
	v_mfma_f32_16x16x32_bf16 v[54:57], v[176:179], v[200:203], v[54:57]
	v_mfma_f32_16x16x32_bf16 v[46:49], v[184:187], v[200:203], v[46:49]
	v_mfma_f32_16x16x32_bf16 v[38:41], v[176:179], v[210:213], v[38:41]
	v_mfma_f32_16x16x32_bf16 v[30:33], v[184:187], v[210:213], v[30:33]
	v_mfma_f32_16x16x32_bf16 v[22:25], v[176:179], v[218:221], v[22:25]
	v_mfma_f32_16x16x32_bf16 v[14:17], v[184:187], v[218:221], v[14:17]
	v_mfma_f32_16x16x32_bf16 v[6:9], v[176:179], v[234:237], v[6:9]
	v_mfma_f32_16x16x32_bf16 v[2:5], v[184:187], v[234:237], v[2:5]
	v_mfma_f32_16x16x32_bf16 v[54:57], v[180:183], v[204:207], v[54:57]
	v_mfma_f32_16x16x32_bf16 v[46:49], v[196:199], v[204:207], v[46:49]
	v_mfma_f32_16x16x32_bf16 v[38:41], v[180:183], v[214:217], v[38:41]
	v_mfma_f32_16x16x32_bf16 v[30:33], v[196:199], v[214:217], v[30:33]
	v_mfma_f32_16x16x32_bf16 v[22:25], v[180:183], v[230:233], v[22:25]
	v_mfma_f32_16x16x32_bf16 v[14:17], v[196:199], v[230:233], v[14:17]
	v_mfma_f32_16x16x32_bf16 v[6:9], v[180:183], v[238:241], v[6:9]
	v_mfma_f32_16x16x32_bf16 v[2:5], v[196:199], v[238:241], v[2:5]
	s_setprio 0
	s_barrier
	s_add_i32 s65, 0, 0x18000
	s_add_i32 s66, 0, 0x1c000
	v_add_u32_e32 v164, s65, v171
	v_add_u32_e32 v175, s66, v171
	ds_read_b128 v[140:143], v164
	ds_read_b128 v[154:157], v164 offset:1024
	ds_read_b128 v[160:163], v164 offset:2048
	ds_read_b128 v[164:167], v164 offset:3072
	ds_read_b128 v[176:179], v175
	ds_read_b128 v[180:183], v175 offset:1024
	ds_read_b128 v[184:187], v175 offset:2048
	ds_read_b128 v[196:199], v175 offset:3072
	s_add_u32 s40, s40, 0x40000
	s_addc_u32 s41, s41, 0
	s_mov_b32 m0, s44
	v_lshl_add_u64 v[208:209], s[40:41], 0, v[146:147]
	ds_read_b128 v[200:203], v173 offset:32768
	ds_read_b128 v[204:207], v173 offset:33792
	ds_read_b128 v[210:213], v173 offset:34816
	ds_read_b128 v[214:217], v173 offset:35840
	ds_read_b128 v[218:221], v173 offset:36864
	ds_read_b128 v[230:233], v173 offset:37888
	ds_read_b128 v[234:237], v173 offset:38912
	ds_read_b128 v[238:241], v173 offset:39936
	global_load_lds_dwordx4 v[208:209], off
	v_lshl_add_u64 v[208:209], s[40:41], 0, v[150:151]
	s_mov_b32 m0, s45
	s_nop 0
	global_load_lds_dwordx4 v[208:209], off
	s_waitcnt vmcnt(8)
	s_waitcnt lgkmcnt(0)
	s_barrier
	s_setprio 1
	s_waitcnt lgkmcnt(0)
	v_mfma_f32_16x16x32_bf16 v[126:129], v[140:143], v[200:203], v[126:129]
	v_mfma_f32_16x16x32_bf16 v[122:125], v[160:163], v[200:203], v[122:125]
	v_mfma_f32_16x16x32_bf16 v[114:117], v[140:143], v[210:213], v[114:117]
	v_mfma_f32_16x16x32_bf16 v[106:109], v[160:163], v[210:213], v[106:109]
	v_mfma_f32_16x16x32_bf16 v[98:101], v[140:143], v[218:221], v[98:101]
	v_mfma_f32_16x16x32_bf16 v[90:93], v[160:163], v[218:221], v[90:93]
	v_mfma_f32_16x16x32_bf16 v[82:85], v[140:143], v[234:237], v[82:85]
	v_mfma_f32_16x16x32_bf16 v[74:77], v[160:163], v[234:237], v[74:77]
	v_mfma_f32_16x16x32_bf16 v[126:129], v[154:157], v[204:207], v[126:129]
	v_mfma_f32_16x16x32_bf16 v[122:125], v[164:167], v[204:207], v[122:125]
	v_mfma_f32_16x16x32_bf16 v[114:117], v[154:157], v[214:217], v[114:117]
	v_mfma_f32_16x16x32_bf16 v[106:109], v[164:167], v[214:217], v[106:109]
	v_mfma_f32_16x16x32_bf16 v[98:101], v[154:157], v[230:233], v[98:101]
	v_mfma_f32_16x16x32_bf16 v[90:93], v[164:167], v[230:233], v[90:93]
	v_mfma_f32_16x16x32_bf16 v[82:85], v[154:157], v[238:241], v[82:85]
	v_mfma_f32_16x16x32_bf16 v[74:77], v[164:167], v[238:241], v[74:77]
	s_setprio 0
	s_setprio 1
	v_mfma_f32_16x16x32_bf16 v[118:121], v[176:179], v[200:203], v[118:121]
	v_mfma_f32_16x16x32_bf16 v[110:113], v[184:187], v[200:203], v[110:113]
	v_mfma_f32_16x16x32_bf16 v[102:105], v[176:179], v[210:213], v[102:105]
	v_mfma_f32_16x16x32_bf16 v[94:97], v[184:187], v[210:213], v[94:97]
	v_mfma_f32_16x16x32_bf16 v[86:89], v[176:179], v[218:221], v[86:89]
	v_mfma_f32_16x16x32_bf16 v[78:81], v[184:187], v[218:221], v[78:81]
	v_mfma_f32_16x16x32_bf16 v[70:73], v[176:179], v[234:237], v[70:73]
	v_mfma_f32_16x16x32_bf16 v[66:69], v[184:187], v[234:237], v[66:69]
	v_mfma_f32_16x16x32_bf16 v[118:121], v[180:183], v[204:207], v[118:121]
	v_mfma_f32_16x16x32_bf16 v[110:113], v[196:199], v[204:207], v[110:113]
	v_mfma_f32_16x16x32_bf16 v[102:105], v[180:183], v[214:217], v[102:105]
	v_mfma_f32_16x16x32_bf16 v[94:97], v[196:199], v[214:217], v[94:97]
	v_mfma_f32_16x16x32_bf16 v[86:89], v[180:183], v[230:233], v[86:89]
	v_mfma_f32_16x16x32_bf16 v[78:81], v[196:199], v[230:233], v[78:81]
	v_mfma_f32_16x16x32_bf16 v[70:73], v[180:183], v[238:241], v[70:73]
	v_mfma_f32_16x16x32_bf16 v[66:69], v[196:199], v[238:241], v[66:69]
	s_setprio 0
	s_barrier
	s_add_i32 s40, s65, s42
	v_lshl_add_u64 v[144:145], v[144:145], 0, s[8:9]
	s_mov_b32 m0, s40
	ds_read_b128 v[200:203], v173 offset:49152
	ds_read_b128 v[204:207], v173 offset:50176
	ds_read_b128 v[210:213], v173 offset:51200
	ds_read_b128 v[214:217], v173 offset:52224
	ds_read_b128 v[218:221], v173 offset:53248
	ds_read_b128 v[230:233], v173 offset:54272
	ds_read_b128 v[234:237], v173 offset:55296
	ds_read_b128 v[238:241], v173 offset:56320
	global_load_lds_dwordx4 v[144:145], off
	s_add_i32 m0, s40, 0x2000
	s_add_u32 s38, s38, 0x10080
	v_lshl_add_u64 v[144:145], v[168:169], 0, s[8:9]
	s_addc_u32 s39, s39, 0
	s_add_i32 s40, s66, s42
	global_load_lds_dwordx4 v[144:145], off
	v_lshl_add_u64 v[144:145], s[38:39], 0, v[148:149]
	s_mov_b32 m0, s40
	s_nop 0
	global_load_lds_dwordx4 v[144:145], off
	v_lshl_add_u64 v[144:145], s[38:39], 0, v[152:153]
	s_add_i32 m0, s40, 0x2000
	s_nop 0
	global_load_lds_dwordx4 v[144:145], off
	v_lshl_add_u64 v[144:145], v[188:189], 0, s[8:9]
	s_mov_b32 m0, s47
	s_nop 0
	global_load_lds_dwordx4 v[144:145], off
	v_lshl_add_u64 v[144:145], v[190:191], 0, s[8:9]
	s_mov_b32 m0, s48
	s_nop 0
	global_load_lds_dwordx4 v[144:145], off
	s_waitcnt vmcnt(8)
	s_waitcnt lgkmcnt(0)
	s_barrier
	s_setprio 1
	s_waitcnt lgkmcnt(0)
	v_mfma_f32_16x16x32_bf16 v[62:65], v[140:143], v[200:203], v[62:65]
	v_mfma_f32_16x16x32_bf16 v[58:61], v[160:163], v[200:203], v[58:61]
	v_mfma_f32_16x16x32_bf16 v[50:53], v[140:143], v[210:213], v[50:53]
	v_mfma_f32_16x16x32_bf16 v[42:45], v[160:163], v[210:213], v[42:45]
	v_mfma_f32_16x16x32_bf16 v[34:37], v[140:143], v[218:221], v[34:37]
	v_mfma_f32_16x16x32_bf16 v[26:29], v[160:163], v[218:221], v[26:29]
	v_mfma_f32_16x16x32_bf16 v[18:21], v[140:143], v[234:237], v[18:21]
	v_mfma_f32_16x16x32_bf16 v[10:13], v[160:163], v[234:237], v[10:13]
	v_mfma_f32_16x16x32_bf16 v[62:65], v[154:157], v[204:207], v[62:65]
	v_mfma_f32_16x16x32_bf16 v[58:61], v[164:167], v[204:207], v[58:61]
	v_mfma_f32_16x16x32_bf16 v[50:53], v[154:157], v[214:217], v[50:53]
	v_mfma_f32_16x16x32_bf16 v[42:45], v[164:167], v[214:217], v[42:45]
	v_mfma_f32_16x16x32_bf16 v[34:37], v[154:157], v[230:233], v[34:37]
	v_mfma_f32_16x16x32_bf16 v[26:29], v[164:167], v[230:233], v[26:29]
	v_mfma_f32_16x16x32_bf16 v[18:21], v[154:157], v[238:241], v[18:21]
	v_mfma_f32_16x16x32_bf16 v[10:13], v[164:167], v[238:241], v[10:13]
	s_setprio 0
	s_setprio 1
	v_mfma_f32_16x16x32_bf16 v[54:57], v[176:179], v[200:203], v[54:57]
	v_mfma_f32_16x16x32_bf16 v[46:49], v[184:187], v[200:203], v[46:49]
	v_mfma_f32_16x16x32_bf16 v[38:41], v[176:179], v[210:213], v[38:41]
	v_mfma_f32_16x16x32_bf16 v[30:33], v[184:187], v[210:213], v[30:33]
	v_mfma_f32_16x16x32_bf16 v[22:25], v[176:179], v[218:221], v[22:25]
	v_mfma_f32_16x16x32_bf16 v[14:17], v[184:187], v[218:221], v[14:17]
	v_mfma_f32_16x16x32_bf16 v[6:9], v[176:179], v[234:237], v[6:9]
	v_mfma_f32_16x16x32_bf16 v[2:5], v[184:187], v[234:237], v[2:5]
	v_mfma_f32_16x16x32_bf16 v[54:57], v[180:183], v[204:207], v[54:57]
	v_mfma_f32_16x16x32_bf16 v[46:49], v[196:199], v[204:207], v[46:49]
	v_mfma_f32_16x16x32_bf16 v[38:41], v[180:183], v[214:217], v[38:41]
	v_mfma_f32_16x16x32_bf16 v[30:33], v[196:199], v[214:217], v[30:33]
	v_mfma_f32_16x16x32_bf16 v[22:25], v[180:183], v[230:233], v[22:25]
	v_mfma_f32_16x16x32_bf16 v[14:17], v[196:199], v[230:233], v[14:17]
	v_mfma_f32_16x16x32_bf16 v[6:9], v[180:183], v[238:241], v[6:9]
	v_mfma_f32_16x16x32_bf16 v[2:5], v[196:199], v[238:241], v[2:5]
	s_setprio 0
	s_add_i32 s64, s64, 2
	s_add_u32 s36, s36, 0x100
	s_addc_u32 s37, s37, 0
	s_add_u32 s62, s62, 0x100
	s_addc_u32 s63, s63, 0
	s_cmp_gt_u32 s64, 13
	s_barrier
	s_cbranch_scc0 .LBB0_1599
	s_and_b64 vcc, exec, s[10:11]
	s_cbranch_vccz .LBB0_1602
	s_barrier

.LBB0_1883:
	ds_read_b128 v[146:149], v164
	ds_read_b128 v[150:153], v164 offset:1024
	ds_read_b128 v[154:157], v164 offset:2048
	ds_read_b128 v[158:161], v164 offset:3072
	ds_read_b128 v[168:171], v165
	ds_read_b128 v[172:175], v165 offset:1024
	ds_read_b128 v[176:179], v165 offset:2048
	ds_read_b128 v[180:183], v165 offset:3072
	s_add_u32 s30, s22, 0xfffc0080
	s_addc_u32 s31, s23, -1
	s_cmp_eq_u32 s52, 12
	s_cselect_b32 s35, s15, s31
	s_cselect_b32 s34, s48, s30
	s_cselect_b32 s31, s13, s51
	s_cselect_b32 s30, s49, s50
	v_lshl_add_u64 v[192:193], s[22:23], 0, v[138:139]
	s_add_i32 m0, s21, 0xc000
	ds_read_b128 v[184:187], v166
	ds_read_b128 v[188:191], v166 offset:1024
	ds_read_b128 v[196:199], v166 offset:2048
	ds_read_b128 v[200:203], v166 offset:3072
	ds_read_b128 v[204:207], v166 offset:4096
	ds_read_b128 v[208:211], v166 offset:5120
	ds_read_b128 v[212:215], v166 offset:6144
	ds_read_b128 v[216:219], v166 offset:7168
	global_load_lds_dwordx4 v[192:193], off
	v_lshl_add_u64 v[192:193], s[22:23], 0, v[140:141]
	s_add_i32 m0, s21, 0xe000
	s_nop 0
	global_load_lds_dwordx4 v[192:193], off
	s_waitcnt vmcnt(8)
	s_waitcnt lgkmcnt(0)
	s_barrier
	s_setprio 1
	s_waitcnt lgkmcnt(0)
	v_mfma_f32_16x16x32_bf16 v[126:129], v[146:149], v[184:187], v[126:129]
	v_mfma_f32_16x16x32_bf16 v[122:125], v[154:157], v[184:187], v[122:125]
	v_mfma_f32_16x16x32_bf16 v[114:117], v[146:149], v[196:199], v[114:117]
	v_mfma_f32_16x16x32_bf16 v[106:109], v[154:157], v[196:199], v[106:109]
	v_mfma_f32_16x16x32_bf16 v[98:101], v[146:149], v[204:207], v[98:101]
	v_mfma_f32_16x16x32_bf16 v[90:93], v[154:157], v[204:207], v[90:93]
	v_mfma_f32_16x16x32_bf16 v[82:85], v[146:149], v[212:215], v[82:85]
	v_mfma_f32_16x16x32_bf16 v[74:77], v[154:157], v[212:215], v[74:77]
	v_mfma_f32_16x16x32_bf16 v[126:129], v[150:153], v[188:191], v[126:129]
	v_mfma_f32_16x16x32_bf16 v[122:125], v[158:161], v[188:191], v[122:125]
	v_mfma_f32_16x16x32_bf16 v[114:117], v[150:153], v[200:203], v[114:117]
	v_mfma_f32_16x16x32_bf16 v[106:109], v[158:161], v[200:203], v[106:109]
	v_mfma_f32_16x16x32_bf16 v[98:101], v[150:153], v[208:211], v[98:101]
	v_mfma_f32_16x16x32_bf16 v[90:93], v[158:161], v[208:211], v[90:93]
	v_mfma_f32_16x16x32_bf16 v[82:85], v[150:153], v[216:219], v[82:85]
	v_mfma_f32_16x16x32_bf16 v[74:77], v[158:161], v[216:219], v[74:77]
	s_setprio 0
	s_setprio 1
	v_mfma_f32_16x16x32_bf16 v[118:121], v[168:171], v[184:187], v[118:121]
	v_mfma_f32_16x16x32_bf16 v[110:113], v[176:179], v[184:187], v[110:113]
	v_mfma_f32_16x16x32_bf16 v[102:105], v[168:171], v[196:199], v[102:105]
	v_mfma_f32_16x16x32_bf16 v[94:97], v[176:179], v[196:199], v[94:97]
	v_mfma_f32_16x16x32_bf16 v[86:89], v[168:171], v[204:207], v[86:89]
	v_mfma_f32_16x16x32_bf16 v[78:81], v[176:179], v[204:207], v[78:81]
	v_mfma_f32_16x16x32_bf16 v[70:73], v[168:171], v[212:215], v[70:73]
	v_mfma_f32_16x16x32_bf16 v[66:69], v[176:179], v[212:215], v[66:69]
	v_mfma_f32_16x16x32_bf16 v[118:121], v[172:175], v[188:191], v[118:121]
	v_mfma_f32_16x16x32_bf16 v[110:113], v[180:183], v[188:191], v[110:113]
	v_mfma_f32_16x16x32_bf16 v[102:105], v[172:175], v[200:203], v[102:105]
	v_mfma_f32_16x16x32_bf16 v[94:97], v[180:183], v[200:203], v[94:97]
	v_mfma_f32_16x16x32_bf16 v[86:89], v[172:175], v[208:211], v[86:89]
	v_mfma_f32_16x16x32_bf16 v[78:81], v[180:183], v[208:211], v[78:81]
	v_mfma_f32_16x16x32_bf16 v[70:73], v[172:175], v[216:219], v[70:73]
	v_mfma_f32_16x16x32_bf16 v[66:69], v[180:183], v[216:219], v[66:69]
	s_setprio 0
	s_barrier
	s_add_i32 s53, s45, s37
	v_lshl_add_u64 v[192:193], s[30:31], 0, v[132:133]
	s_mov_b32 m0, s53
	ds_read_b128 v[184:187], v166 offset:16384
	ds_read_b128 v[188:191], v166 offset:17408
	ds_read_b128 v[196:199], v166 offset:18432
	ds_read_b128 v[200:203], v166 offset:19456
	ds_read_b128 v[204:207], v166 offset:20480
	ds_read_b128 v[208:211], v166 offset:21504
	ds_read_b128 v[212:215], v166 offset:22528
	ds_read_b128 v[216:219], v166 offset:23552
	global_load_lds_dwordx4 v[192:193], off
	s_add_i32 m0, s53, 0x2000
	s_add_u32 s54, s30, 0x40000
	v_lshl_add_u64 v[220:221], s[30:31], 0, v[136:137]
	s_addc_u32 s55, s31, 0
	s_add_i32 s53, s46, s37
	global_load_lds_dwordx4 v[220:221], off
	v_lshl_add_u64 v[230:231], s[54:55], 0, v[132:133]
	s_mov_b32 m0, s53
	v_lshl_add_u64 v[232:233], s[34:35], 0, v[134:135]
	global_load_lds_dwordx4 v[230:231], off
	v_lshl_add_u64 v[230:231], s[54:55], 0, v[136:137]
	s_add_i32 m0, s53, 0x2000
	s_nop 0
	global_load_lds_dwordx4 v[230:231], off
	v_lshl_add_u64 v[230:231], s[34:35], 0, v[130:131]
	s_mov_b32 m0, s21
	s_nop 0
	global_load_lds_dwordx4 v[230:231], off
	s_mov_b32 m0, s38
	s_nop 0
	global_load_lds_dwordx4 v[232:233], off
	s_waitcnt vmcnt(8)
	s_waitcnt lgkmcnt(0)
	s_barrier
	s_setprio 1
	s_waitcnt lgkmcnt(0)
	v_mfma_f32_16x16x32_bf16 v[62:65], v[146:149], v[184:187], v[62:65]
	v_mfma_f32_16x16x32_bf16 v[58:61], v[154:157], v[184:187], v[58:61]
	v_mfma_f32_16x16x32_bf16 v[50:53], v[146:149], v[196:199], v[50:53]
	v_mfma_f32_16x16x32_bf16 v[42:45], v[154:157], v[196:199], v[42:45]
	v_mfma_f32_16x16x32_bf16 v[34:37], v[146:149], v[204:207], v[34:37]
	v_mfma_f32_16x16x32_bf16 v[26:29], v[154:157], v[204:207], v[26:29]
	v_mfma_f32_16x16x32_bf16 v[18:21], v[146:149], v[212:215], v[18:21]
	v_mfma_f32_16x16x32_bf16 v[10:13], v[154:157], v[212:215], v[10:13]
	v_mfma_f32_16x16x32_bf16 v[62:65], v[150:153], v[188:191], v[62:65]
	v_mfma_f32_16x16x32_bf16 v[58:61], v[158:161], v[188:191], v[58:61]
	v_mfma_f32_16x16x32_bf16 v[50:53], v[150:153], v[200:203], v[50:53]
	v_mfma_f32_16x16x32_bf16 v[42:45], v[158:161], v[200:203], v[42:45]
	v_mfma_f32_16x16x32_bf16 v[34:37], v[150:153], v[208:211], v[34:37]
	v_mfma_f32_16x16x32_bf16 v[26:29], v[158:161], v[208:211], v[26:29]
	v_mfma_f32_16x16x32_bf16 v[18:21], v[150:153], v[216:219], v[18:21]
	v_mfma_f32_16x16x32_bf16 v[10:13], v[158:161], v[216:219], v[10:13]
	s_setprio 0
	s_setprio 1
	v_mfma_f32_16x16x32_bf16 v[54:57], v[168:171], v[184:187], v[54:57]
	v_mfma_f32_16x16x32_bf16 v[46:49], v[176:179], v[184:187], v[46:49]
	v_mfma_f32_16x16x32_bf16 v[38:41], v[168:171], v[196:199], v[38:41]
	v_mfma_f32_16x16x32_bf16 v[30:33], v[176:179], v[196:199], v[30:33]
	v_mfma_f32_16x16x32_bf16 v[22:25], v[168:171], v[204:207], v[22:25]
	v_mfma_f32_16x16x32_bf16 v[14:17], v[176:179], v[204:207], v[14:17]
	v_mfma_f32_16x16x32_bf16 v[6:9], v[168:171], v[212:215], v[6:9]
	v_mfma_f32_16x16x32_bf16 v[2:5], v[176:179], v[212:215], v[2:5]
	v_mfma_f32_16x16x32_bf16 v[54:57], v[172:175], v[188:191], v[54:57]
	v_mfma_f32_16x16x32_bf16 v[46:49], v[180:183], v[188:191], v[46:49]
	v_mfma_f32_16x16x32_bf16 v[38:41], v[172:175], v[200:203], v[38:41]
	v_mfma_f32_16x16x32_bf16 v[30:33], v[180:183], v[200:203], v[30:33]
	v_mfma_f32_16x16x32_bf16 v[22:25], v[172:175], v[208:211], v[22:25]
	v_mfma_f32_16x16x32_bf16 v[14:17], v[180:183], v[208:211], v[14:17]
	v_mfma_f32_16x16x32_bf16 v[6:9], v[172:175], v[216:219], v[6:9]
	v_mfma_f32_16x16x32_bf16 v[2:5], v[180:183], v[216:219], v[2:5]
	s_setprio 0
	s_barrier
	s_add_i32 s53, 0, 0x18000
	s_add_i32 s54, 0, 0x1c000
	v_add_u32_e32 v158, s53, v162
	v_add_u32_e32 v167, s54, v162
	ds_read_b128 v[146:149], v158
	ds_read_b128 v[150:153], v158 offset:1024
	ds_read_b128 v[154:157], v158 offset:2048
	ds_read_b128 v[158:161], v158 offset:3072
	ds_read_b128 v[168:171], v167
	ds_read_b128 v[172:175], v167 offset:1024
	ds_read_b128 v[176:179], v167 offset:2048
	ds_read_b128 v[180:183], v167 offset:3072
	s_add_u32 s34, s34, 0x40000
	s_addc_u32 s35, s35, 0
	s_mov_b32 m0, s39
	v_lshl_add_u64 v[234:235], s[34:35], 0, v[130:131]
	ds_read_b128 v[184:187], v166 offset:32768
	ds_read_b128 v[188:191], v166 offset:33792
	ds_read_b128 v[196:199], v166 offset:34816
	ds_read_b128 v[200:203], v166 offset:35840
	ds_read_b128 v[204:207], v166 offset:36864
	ds_read_b128 v[208:211], v166 offset:37888
	ds_read_b128 v[212:215], v166 offset:38912
	ds_read_b128 v[216:219], v166 offset:39936
	global_load_lds_dwordx4 v[234:235], off
	v_lshl_add_u64 v[234:235], s[34:35], 0, v[134:135]
	s_mov_b32 m0, s40
	s_nop 0
	global_load_lds_dwordx4 v[234:235], off
	s_waitcnt vmcnt(8)
	s_waitcnt lgkmcnt(0)
	s_barrier
	s_setprio 1
	s_waitcnt lgkmcnt(0)
	v_mfma_f32_16x16x32_bf16 v[126:129], v[146:149], v[184:187], v[126:129]
	v_mfma_f32_16x16x32_bf16 v[122:125], v[154:157], v[184:187], v[122:125]
	v_mfma_f32_16x16x32_bf16 v[114:117], v[146:149], v[196:199], v[114:117]
	v_mfma_f32_16x16x32_bf16 v[106:109], v[154:157], v[196:199], v[106:109]
	v_mfma_f32_16x16x32_bf16 v[98:101], v[146:149], v[204:207], v[98:101]
	v_mfma_f32_16x16x32_bf16 v[90:93], v[154:157], v[204:207], v[90:93]
	v_mfma_f32_16x16x32_bf16 v[82:85], v[146:149], v[212:215], v[82:85]
	v_mfma_f32_16x16x32_bf16 v[74:77], v[154:157], v[212:215], v[74:77]
	v_mfma_f32_16x16x32_bf16 v[126:129], v[150:153], v[188:191], v[126:129]
	v_mfma_f32_16x16x32_bf16 v[122:125], v[158:161], v[188:191], v[122:125]
	v_mfma_f32_16x16x32_bf16 v[114:117], v[150:153], v[200:203], v[114:117]
	v_mfma_f32_16x16x32_bf16 v[106:109], v[158:161], v[200:203], v[106:109]
	v_mfma_f32_16x16x32_bf16 v[98:101], v[150:153], v[208:211], v[98:101]
	v_mfma_f32_16x16x32_bf16 v[90:93], v[158:161], v[208:211], v[90:93]
	v_mfma_f32_16x16x32_bf16 v[82:85], v[150:153], v[216:219], v[82:85]
	v_mfma_f32_16x16x32_bf16 v[74:77], v[158:161], v[216:219], v[74:77]
	s_setprio 0
	s_setprio 1
	v_mfma_f32_16x16x32_bf16 v[118:121], v[168:171], v[184:187], v[118:121]
	v_mfma_f32_16x16x32_bf16 v[110:113], v[176:179], v[184:187], v[110:113]
	v_mfma_f32_16x16x32_bf16 v[102:105], v[168:171], v[196:199], v[102:105]
	v_mfma_f32_16x16x32_bf16 v[94:97], v[176:179], v[196:199], v[94:97]
	v_mfma_f32_16x16x32_bf16 v[86:89], v[168:171], v[204:207], v[86:89]
	v_mfma_f32_16x16x32_bf16 v[78:81], v[176:179], v[204:207], v[78:81]
	v_mfma_f32_16x16x32_bf16 v[70:73], v[168:171], v[212:215], v[70:73]
	v_mfma_f32_16x16x32_bf16 v[66:69], v[176:179], v[212:215], v[66:69]
	v_mfma_f32_16x16x32_bf16 v[118:121], v[172:175], v[188:191], v[118:121]
	v_mfma_f32_16x16x32_bf16 v[110:113], v[180:183], v[188:191], v[110:113]
	v_mfma_f32_16x16x32_bf16 v[102:105], v[172:175], v[200:203], v[102:105]
	v_mfma_f32_16x16x32_bf16 v[94:97], v[180:183], v[200:203], v[94:97]
	v_mfma_f32_16x16x32_bf16 v[86:89], v[172:175], v[208:211], v[86:89]
	v_mfma_f32_16x16x32_bf16 v[78:81], v[180:183], v[208:211], v[78:81]
	v_mfma_f32_16x16x32_bf16 v[70:73], v[172:175], v[216:219], v[70:73]
	v_mfma_f32_16x16x32_bf16 v[66:69], v[180:183], v[216:219], v[66:69]
	s_setprio 0
	s_barrier
	s_add_i32 s34, s53, s37
	v_lshl_add_u64 v[192:193], v[192:193], 0, s[8:9]
	s_mov_b32 m0, s34
	ds_read_b128 v[184:187], v166 offset:49152
	ds_read_b128 v[188:191], v166 offset:50176
	ds_read_b128 v[196:199], v166 offset:51200
	ds_read_b128 v[200:203], v166 offset:52224
	ds_read_b128 v[204:207], v166 offset:53248
	ds_read_b128 v[208:211], v166 offset:54272
	ds_read_b128 v[212:215], v166 offset:55296
	ds_read_b128 v[216:219], v166 offset:56320
	global_load_lds_dwordx4 v[192:193], off
	s_add_i32 m0, s34, 0x2000
	s_add_u32 s30, s30, 0x40080
	v_lshl_add_u64 v[192:193], v[220:221], 0, s[8:9]
	s_addc_u32 s31, s31, 0
	s_add_i32 s34, s54, s37
	global_load_lds_dwordx4 v[192:193], off
	v_lshl_add_u64 v[192:193], s[30:31], 0, v[132:133]
	s_mov_b32 m0, s34
	s_nop 0
	global_load_lds_dwordx4 v[192:193], off
	v_lshl_add_u64 v[192:193], s[30:31], 0, v[136:137]
	s_add_i32 m0, s34, 0x2000
	s_nop 0
	global_load_lds_dwordx4 v[192:193], off
	v_lshl_add_u64 v[192:193], v[230:231], 0, s[8:9]
	s_mov_b32 m0, s42
	s_nop 0
	global_load_lds_dwordx4 v[192:193], off
	v_lshl_add_u64 v[192:193], v[232:233], 0, s[8:9]
	s_mov_b32 m0, s43
	s_nop 0
	global_load_lds_dwordx4 v[192:193], off
	s_waitcnt vmcnt(8)
	s_waitcnt lgkmcnt(0)
	s_barrier
	s_setprio 1
	s_waitcnt lgkmcnt(0)
	v_mfma_f32_16x16x32_bf16 v[62:65], v[146:149], v[184:187], v[62:65]
	v_mfma_f32_16x16x32_bf16 v[58:61], v[154:157], v[184:187], v[58:61]
	v_mfma_f32_16x16x32_bf16 v[50:53], v[146:149], v[196:199], v[50:53]
	v_mfma_f32_16x16x32_bf16 v[42:45], v[154:157], v[196:199], v[42:45]
	v_mfma_f32_16x16x32_bf16 v[34:37], v[146:149], v[204:207], v[34:37]
	v_mfma_f32_16x16x32_bf16 v[26:29], v[154:157], v[204:207], v[26:29]
	v_mfma_f32_16x16x32_bf16 v[18:21], v[146:149], v[212:215], v[18:21]
	v_mfma_f32_16x16x32_bf16 v[10:13], v[154:157], v[212:215], v[10:13]
	v_mfma_f32_16x16x32_bf16 v[62:65], v[150:153], v[188:191], v[62:65]
	v_mfma_f32_16x16x32_bf16 v[58:61], v[158:161], v[188:191], v[58:61]
	v_mfma_f32_16x16x32_bf16 v[50:53], v[150:153], v[200:203], v[50:53]
	v_mfma_f32_16x16x32_bf16 v[42:45], v[158:161], v[200:203], v[42:45]
	v_mfma_f32_16x16x32_bf16 v[34:37], v[150:153], v[208:211], v[34:37]
	v_mfma_f32_16x16x32_bf16 v[26:29], v[158:161], v[208:211], v[26:29]
	v_mfma_f32_16x16x32_bf16 v[18:21], v[150:153], v[216:219], v[18:21]
	v_mfma_f32_16x16x32_bf16 v[10:13], v[158:161], v[216:219], v[10:13]
	s_setprio 0
	s_setprio 1
	v_mfma_f32_16x16x32_bf16 v[54:57], v[168:171], v[184:187], v[54:57]
	v_mfma_f32_16x16x32_bf16 v[46:49], v[176:179], v[184:187], v[46:49]
	v_mfma_f32_16x16x32_bf16 v[38:41], v[168:171], v[196:199], v[38:41]
	v_mfma_f32_16x16x32_bf16 v[30:33], v[176:179], v[196:199], v[30:33]
	v_mfma_f32_16x16x32_bf16 v[22:25], v[168:171], v[204:207], v[22:25]
	v_mfma_f32_16x16x32_bf16 v[14:17], v[176:179], v[204:207], v[14:17]
	v_mfma_f32_16x16x32_bf16 v[6:9], v[168:171], v[212:215], v[6:9]
	v_mfma_f32_16x16x32_bf16 v[2:5], v[176:179], v[212:215], v[2:5]
	v_mfma_f32_16x16x32_bf16 v[54:57], v[172:175], v[188:191], v[54:57]
	v_mfma_f32_16x16x32_bf16 v[46:49], v[180:183], v[188:191], v[46:49]
	v_mfma_f32_16x16x32_bf16 v[38:41], v[172:175], v[200:203], v[38:41]
	v_mfma_f32_16x16x32_bf16 v[30:33], v[180:183], v[200:203], v[30:33]
	v_mfma_f32_16x16x32_bf16 v[22:25], v[172:175], v[208:211], v[22:25]
	v_mfma_f32_16x16x32_bf16 v[14:17], v[180:183], v[208:211], v[14:17]
	v_mfma_f32_16x16x32_bf16 v[6:9], v[172:175], v[216:219], v[6:9]
	v_mfma_f32_16x16x32_bf16 v[2:5], v[180:183], v[216:219], v[2:5]
	s_setprio 0
	s_add_i32 s52, s52, 2
	s_add_u32 s22, s22, 0x100
	s_addc_u32 s23, s23, 0
	s_add_u32 s50, s50, 0x100
	s_addc_u32 s51, s51, 0
	s_cmp_gt_u32 s52, 13
	s_barrier
	s_cbranch_scc0 .LBB0_1883
	s_and_b64 vcc, exec, s[10:11]
	s_cbranch_vccz .LBB0_1886
	s_barrier

.LBB0_2074:
	ds_read_b128 v[166:169], v162
	ds_read_b128 v[170:173], v162 offset:1024
	ds_read_b128 v[174:177], v162 offset:2048
	ds_read_b128 v[178:181], v162 offset:3072
	ds_read_b128 v[182:185], v163
	ds_read_b128 v[186:189], v163 offset:1024
	ds_read_b128 v[190:193], v163 offset:2048
	ds_read_b128 v[194:197], v163 offset:3072
	s_add_u32 s18, s16, 0x80
	s_addc_u32 s19, s17, 0
	s_cmp_eq_u32 s58, 12
	s_cselect_b32 s19, s83, s19
	s_cselect_b32 s18, s82, s18
	s_cselect_b32 s21, s13, s57
	s_cselect_b32 s20, s12, s56
	s_cselect_b32 s59, s55, s54
	ds_read_b128 v[198:201], v164 offset:1024
	ds_read_b128 v[202:205], v164 offset:2048
	ds_read_b128 v[206:209], v164 offset:3072
	ds_read_b128 v[210:213], v164 offset:4096
	ds_read_b128 v[214:217], v164
	ds_read2_b32 v[232:233], v165 offset0:2 offset1:3
	ds_read_b128 v[218:221], v164 offset:5120
	ds_read_b128 v[224:227], v164 offset:6144
	ds_read_b128 v[228:231], v164 offset:7168
	s_add_i32 m0, s35, 0xc000
	s_waitcnt lgkmcnt(0)
	global_load_lds_dwordx4 v232, s[16:17]
	s_add_i32 m0, s35, 0xe000
	s_nop 0
	global_load_lds_dwordx4 v233, s[16:17]
	s_waitcnt vmcnt(8)
	s_waitcnt lgkmcnt(0)
	s_barrier
	s_setprio 1
	v_mfma_f32_16x16x32_bf16 v[126:129], v[166:169], v[214:217], v[126:129]
	v_mfma_f32_16x16x32_bf16 v[122:125], v[174:177], v[214:217], v[122:125]
	v_mfma_f32_16x16x32_bf16 v[94:97], v[166:169], v[202:205], v[94:97]
	v_mfma_f32_16x16x32_bf16 v[82:85], v[174:177], v[202:205], v[82:85]
	v_mfma_f32_16x16x32_bf16 v[54:57], v[166:169], v[210:213], v[54:57]
	v_mfma_f32_16x16x32_bf16 v[42:45], v[174:177], v[210:213], v[42:45]
	v_mfma_f32_16x16x32_bf16 v[18:21], v[166:169], v[224:227], v[18:21]
	v_mfma_f32_16x16x32_bf16 v[10:13], v[174:177], v[224:227], v[10:13]
	v_mfma_f32_16x16x32_bf16 v[126:129], v[170:173], v[198:201], v[126:129]
	v_mfma_f32_16x16x32_bf16 v[122:125], v[178:181], v[198:201], v[122:125]
	v_mfma_f32_16x16x32_bf16 v[94:97], v[170:173], v[206:209], v[94:97]
	v_mfma_f32_16x16x32_bf16 v[82:85], v[178:181], v[206:209], v[82:85]
	v_mfma_f32_16x16x32_bf16 v[54:57], v[170:173], v[218:221], v[54:57]
	v_mfma_f32_16x16x32_bf16 v[42:45], v[178:181], v[218:221], v[42:45]
	v_mfma_f32_16x16x32_bf16 v[18:21], v[170:173], v[228:231], v[18:21]
	v_mfma_f32_16x16x32_bf16 v[10:13], v[178:181], v[228:231], v[10:13]
	s_setprio 0
	s_setprio 1
	v_mfma_f32_16x16x32_bf16 v[102:105], v[182:185], v[214:217], v[102:105]
	v_mfma_f32_16x16x32_bf16 v[98:101], v[190:193], v[214:217], v[98:101]
	v_mfma_f32_16x16x32_bf16 v[70:73], v[182:185], v[202:205], v[70:73]
	v_mfma_f32_16x16x32_bf16 v[66:69], v[190:193], v[202:205], v[66:69]
	v_mfma_f32_16x16x32_bf16 v[38:41], v[182:185], v[210:213], v[38:41]
	v_mfma_f32_16x16x32_bf16 v[34:37], v[190:193], v[210:213], v[34:37]
	v_mfma_f32_16x16x32_bf16 v[6:9], v[182:185], v[224:227], v[6:9]
	v_mfma_f32_16x16x32_bf16 v[2:5], v[190:193], v[224:227], v[2:5]
	v_mfma_f32_16x16x32_bf16 v[102:105], v[186:189], v[198:201], v[102:105]
	v_mfma_f32_16x16x32_bf16 v[98:101], v[194:197], v[198:201], v[98:101]
	v_mfma_f32_16x16x32_bf16 v[70:73], v[186:189], v[206:209], v[70:73]
	v_mfma_f32_16x16x32_bf16 v[66:69], v[194:197], v[206:209], v[66:69]
	v_mfma_f32_16x16x32_bf16 v[38:41], v[186:189], v[218:221], v[38:41]
	v_mfma_f32_16x16x32_bf16 v[34:37], v[194:197], v[218:221], v[34:37]
	v_mfma_f32_16x16x32_bf16 v[6:9], v[186:189], v[228:231], v[6:9]
	v_mfma_f32_16x16x32_bf16 v[2:5], v[194:197], v[228:231], v[2:5]
	s_setprio 0
	s_barrier
	s_add_i32 s62, s41, s34
	v_lshl_add_u64 v[232:233], s[20:21], 0, v[134:135]
	s_mov_b32 m0, s62
	ds_read_b128 v[198:201], v164 offset:16384
	ds_read_b128 v[202:205], v164 offset:17408
	ds_read_b128 v[206:209], v164 offset:18432
	ds_read_b128 v[210:213], v164 offset:19456
	ds_read_b128 v[214:217], v164 offset:20480
	ds_read_b128 v[218:221], v164 offset:21504
	ds_read_b128 v[224:227], v164 offset:22528
	ds_read_b128 v[228:231], v164 offset:23552
	global_load_lds_dwordx4 v[232:233], off
	s_add_i32 m0, s62, 0x2000
	s_add_u32 s62, s20, 0x40000
	v_lshl_add_u64 v[234:235], s[20:21], 0, v[132:133]
	s_addc_u32 s63, s21, 0
	s_add_i32 s64, s42, s34
	global_load_lds_dwordx4 v[234:235], off
	v_lshl_add_u64 v[236:237], s[62:63], 0, v[134:135]
	s_mov_b32 m0, s64
	v_lshl_add_u32 v136, s59, 2, v149
	global_load_lds_dwordx4 v[236:237], off
	v_lshl_add_u64 v[236:237], s[62:63], 0, v[132:133]
	s_add_i32 m0, s64, 0x2000
	s_nop 0
	global_load_lds_dwordx4 v[236:237], off
	ds_read2_b32 v[236:237], v136 offset1:1
	s_mov_b32 m0, s35
	s_waitcnt lgkmcnt(0)
	global_load_lds_dwordx4 v236, s[18:19]
	s_mov_b32 m0, s36
	s_nop 0
	global_load_lds_dwordx4 v237, s[18:19]
	s_waitcnt vmcnt(8)
	s_waitcnt lgkmcnt(0)
	s_barrier
	s_setprio 1
	v_mfma_f32_16x16x32_bf16 v[118:121], v[166:169], v[198:201], v[118:121]
	v_mfma_f32_16x16x32_bf16 v[114:117], v[174:177], v[198:201], v[114:117]
	v_mfma_f32_16x16x32_bf16 v[90:93], v[166:169], v[206:209], v[90:93]
	v_mfma_f32_16x16x32_bf16 v[86:89], v[174:177], v[206:209], v[86:89]
	v_mfma_f32_16x16x32_bf16 v[62:65], v[166:169], v[214:217], v[62:65]
	v_mfma_f32_16x16x32_bf16 v[58:61], v[174:177], v[214:217], v[58:61]
	v_mfma_f32_16x16x32_bf16 v[30:33], v[166:169], v[224:227], v[30:33]
	v_mfma_f32_16x16x32_bf16 v[26:29], v[174:177], v[224:227], v[26:29]
	v_mfma_f32_16x16x32_bf16 v[118:121], v[170:173], v[202:205], v[118:121]
	v_mfma_f32_16x16x32_bf16 v[114:117], v[178:181], v[202:205], v[114:117]
	v_mfma_f32_16x16x32_bf16 v[90:93], v[170:173], v[210:213], v[90:93]
	v_mfma_f32_16x16x32_bf16 v[86:89], v[178:181], v[210:213], v[86:89]
	v_mfma_f32_16x16x32_bf16 v[62:65], v[170:173], v[218:221], v[62:65]
	v_mfma_f32_16x16x32_bf16 v[58:61], v[178:181], v[218:221], v[58:61]
	v_mfma_f32_16x16x32_bf16 v[30:33], v[170:173], v[228:231], v[30:33]
	v_mfma_f32_16x16x32_bf16 v[26:29], v[178:181], v[228:231], v[26:29]
	s_setprio 0
	s_setprio 1
	v_mfma_f32_16x16x32_bf16 v[110:113], v[182:185], v[198:201], v[110:113]
	v_mfma_f32_16x16x32_bf16 v[106:109], v[190:193], v[198:201], v[106:109]
	v_mfma_f32_16x16x32_bf16 v[78:81], v[182:185], v[206:209], v[78:81]
	v_mfma_f32_16x16x32_bf16 v[74:77], v[190:193], v[206:209], v[74:77]
	v_mfma_f32_16x16x32_bf16 v[50:53], v[182:185], v[214:217], v[50:53]
	v_mfma_f32_16x16x32_bf16 v[46:49], v[190:193], v[214:217], v[46:49]
	v_mfma_f32_16x16x32_bf16 v[22:25], v[182:185], v[224:227], v[22:25]
	v_mfma_f32_16x16x32_bf16 v[14:17], v[190:193], v[224:227], v[14:17]
	v_mfma_f32_16x16x32_bf16 v[110:113], v[186:189], v[202:205], v[110:113]
	v_mfma_f32_16x16x32_bf16 v[106:109], v[194:197], v[202:205], v[106:109]
	v_mfma_f32_16x16x32_bf16 v[78:81], v[186:189], v[210:213], v[78:81]
	v_mfma_f32_16x16x32_bf16 v[74:77], v[194:197], v[210:213], v[74:77]
	v_mfma_f32_16x16x32_bf16 v[50:53], v[186:189], v[218:221], v[50:53]
	v_mfma_f32_16x16x32_bf16 v[46:49], v[194:197], v[218:221], v[46:49]
	v_mfma_f32_16x16x32_bf16 v[22:25], v[186:189], v[228:231], v[22:25]
	v_mfma_f32_16x16x32_bf16 v[14:17], v[194:197], v[228:231], v[14:17]
	s_setprio 0
	s_barrier
	s_add_i32 s59, 0, 0x18000
	s_add_i32 s62, 0, 0x1c000
	v_add_u32_e32 v178, s59, v151
	v_add_u32_e32 v194, s62, v151
	ds_read_b128 v[166:169], v178
	ds_read_b128 v[170:173], v178 offset:1024
	ds_read_b128 v[174:177], v178 offset:2048
	ds_read_b128 v[178:181], v178 offset:3072
	ds_read_b128 v[182:185], v194
	ds_read_b128 v[186:189], v194 offset:1024
	ds_read_b128 v[190:193], v194 offset:2048
	ds_read_b128 v[194:197], v194 offset:3072
	ds_read_b128 v[198:201], v164 offset:32768
	ds_read_b128 v[202:205], v164 offset:33792
	ds_read_b128 v[206:209], v164 offset:34816
	ds_read_b128 v[210:213], v164 offset:35840
	ds_read_b128 v[214:217], v164 offset:36864
	ds_read_b128 v[218:221], v164 offset:37888
	ds_read2_b32 v[236:237], v136 offset0:2 offset1:3
	ds_read_b128 v[224:227], v164 offset:38912
	ds_read_b128 v[228:231], v164 offset:39936
	s_mov_b32 m0, s37
	s_waitcnt lgkmcnt(0)
	global_load_lds_dwordx4 v236, s[18:19]
	s_mov_b32 m0, s38
	s_nop 0
	global_load_lds_dwordx4 v237, s[18:19]
	s_waitcnt vmcnt(8)
	s_waitcnt lgkmcnt(0)
	s_barrier
	s_setprio 1
	v_mfma_f32_16x16x32_bf16 v[126:129], v[166:169], v[198:201], v[126:129]
	v_mfma_f32_16x16x32_bf16 v[122:125], v[174:177], v[198:201], v[122:125]
	v_mfma_f32_16x16x32_bf16 v[94:97], v[166:169], v[206:209], v[94:97]
	v_mfma_f32_16x16x32_bf16 v[82:85], v[174:177], v[206:209], v[82:85]
	v_mfma_f32_16x16x32_bf16 v[54:57], v[166:169], v[214:217], v[54:57]
	v_mfma_f32_16x16x32_bf16 v[42:45], v[174:177], v[214:217], v[42:45]
	v_mfma_f32_16x16x32_bf16 v[18:21], v[166:169], v[224:227], v[18:21]
	v_mfma_f32_16x16x32_bf16 v[10:13], v[174:177], v[224:227], v[10:13]
	v_mfma_f32_16x16x32_bf16 v[126:129], v[170:173], v[202:205], v[126:129]
	v_mfma_f32_16x16x32_bf16 v[122:125], v[178:181], v[202:205], v[122:125]
	v_mfma_f32_16x16x32_bf16 v[94:97], v[170:173], v[210:213], v[94:97]
	v_mfma_f32_16x16x32_bf16 v[82:85], v[178:181], v[210:213], v[82:85]
	v_mfma_f32_16x16x32_bf16 v[54:57], v[170:173], v[218:221], v[54:57]
	v_mfma_f32_16x16x32_bf16 v[42:45], v[178:181], v[218:221], v[42:45]
	v_mfma_f32_16x16x32_bf16 v[18:21], v[170:173], v[228:231], v[18:21]
	v_mfma_f32_16x16x32_bf16 v[10:13], v[178:181], v[228:231], v[10:13]
	s_setprio 0
	s_setprio 1
	v_mfma_f32_16x16x32_bf16 v[102:105], v[182:185], v[198:201], v[102:105]
	v_mfma_f32_16x16x32_bf16 v[98:101], v[190:193], v[198:201], v[98:101]
	v_mfma_f32_16x16x32_bf16 v[70:73], v[182:185], v[206:209], v[70:73]
	v_mfma_f32_16x16x32_bf16 v[66:69], v[190:193], v[206:209], v[66:69]
	v_mfma_f32_16x16x32_bf16 v[38:41], v[182:185], v[214:217], v[38:41]
	v_mfma_f32_16x16x32_bf16 v[34:37], v[190:193], v[214:217], v[34:37]
	v_mfma_f32_16x16x32_bf16 v[6:9], v[182:185], v[224:227], v[6:9]
	v_mfma_f32_16x16x32_bf16 v[2:5], v[190:193], v[224:227], v[2:5]
	v_mfma_f32_16x16x32_bf16 v[102:105], v[186:189], v[202:205], v[102:105]
	v_mfma_f32_16x16x32_bf16 v[98:101], v[194:197], v[202:205], v[98:101]
	v_mfma_f32_16x16x32_bf16 v[70:73], v[186:189], v[210:213], v[70:73]
	v_mfma_f32_16x16x32_bf16 v[66:69], v[194:197], v[210:213], v[66:69]
	v_mfma_f32_16x16x32_bf16 v[38:41], v[186:189], v[218:221], v[38:41]
	v_mfma_f32_16x16x32_bf16 v[34:37], v[194:197], v[218:221], v[34:37]
	v_mfma_f32_16x16x32_bf16 v[6:9], v[186:189], v[228:231], v[6:9]
	v_mfma_f32_16x16x32_bf16 v[2:5], v[194:197], v[228:231], v[2:5]
	s_setprio 0
	s_barrier
	s_add_i32 s59, s59, s34
	v_lshl_add_u64 v[232:233], v[232:233], 0, s[6:7]
	s_mov_b32 m0, s59
	ds_read_b128 v[198:201], v164 offset:49152
	ds_read_b128 v[202:205], v164 offset:50176
	ds_read_b128 v[206:209], v164 offset:51200
	ds_read_b128 v[210:213], v164 offset:52224
	ds_read_b128 v[214:217], v164 offset:53248
	ds_read_b128 v[218:221], v164 offset:54272
	ds_read_b128 v[224:227], v164 offset:55296
	ds_read_b128 v[228:231], v164 offset:56320
	global_load_lds_dwordx4 v[232:233], off
	s_add_i32 m0, s59, 0x2000
	s_add_u32 s20, s20, 0x40080
	v_lshl_add_u64 v[232:233], v[234:235], 0, s[6:7]
	s_addc_u32 s21, s21, 0
	s_add_i32 s59, s62, s34
	global_load_lds_dwordx4 v[232:233], off
	v_lshl_add_u64 v[232:233], s[20:21], 0, v[134:135]
	s_mov_b32 m0, s59
	s_nop 0
	global_load_lds_dwordx4 v[232:233], off
	v_lshl_add_u64 v[232:233], s[20:21], 0, v[132:133]
	s_add_i32 m0, s59, 0x2000
	s_nop 0
	global_load_lds_dwordx4 v[232:233], off
	ds_read2_b32 v[232:233], v136 offset1:1
	s_mov_b32 m0, s39
	s_waitcnt lgkmcnt(0)
	v_mov_b32_e32 v136, v232
	v_lshl_add_u64 v[234:235], s[18:19], 0, v[136:137]
	v_mov_b32_e32 v136, v233
	v_lshl_add_u64 v[234:235], v[234:235], 0, s[6:7]
	v_lshl_add_u64 v[232:233], s[18:19], 0, v[136:137]
	global_load_lds_dwordx4 v[234:235], off
	v_lshl_add_u64 v[232:233], v[232:233], 0, s[6:7]
	s_mov_b32 m0, s40
	s_nop 0
	global_load_lds_dwordx4 v[232:233], off
	s_waitcnt vmcnt(8)
	s_waitcnt lgkmcnt(0)
	s_barrier
	s_setprio 1
	v_mfma_f32_16x16x32_bf16 v[118:121], v[166:169], v[198:201], v[118:121]
	v_mfma_f32_16x16x32_bf16 v[114:117], v[174:177], v[198:201], v[114:117]
	v_mfma_f32_16x16x32_bf16 v[90:93], v[166:169], v[206:209], v[90:93]
	v_mfma_f32_16x16x32_bf16 v[86:89], v[174:177], v[206:209], v[86:89]
	v_mfma_f32_16x16x32_bf16 v[62:65], v[166:169], v[214:217], v[62:65]
	v_mfma_f32_16x16x32_bf16 v[58:61], v[174:177], v[214:217], v[58:61]
	v_mfma_f32_16x16x32_bf16 v[30:33], v[166:169], v[224:227], v[30:33]
	v_mfma_f32_16x16x32_bf16 v[26:29], v[174:177], v[224:227], v[26:29]
	v_mfma_f32_16x16x32_bf16 v[118:121], v[170:173], v[202:205], v[118:121]
	v_mfma_f32_16x16x32_bf16 v[114:117], v[178:181], v[202:205], v[114:117]
	v_mfma_f32_16x16x32_bf16 v[90:93], v[170:173], v[210:213], v[90:93]
	v_mfma_f32_16x16x32_bf16 v[86:89], v[178:181], v[210:213], v[86:89]
	v_mfma_f32_16x16x32_bf16 v[62:65], v[170:173], v[218:221], v[62:65]
	v_mfma_f32_16x16x32_bf16 v[58:61], v[178:181], v[218:221], v[58:61]
	v_mfma_f32_16x16x32_bf16 v[30:33], v[170:173], v[228:231], v[30:33]
	v_mfma_f32_16x16x32_bf16 v[26:29], v[178:181], v[228:231], v[26:29]
	s_setprio 0
	s_setprio 1
	v_mfma_f32_16x16x32_bf16 v[110:113], v[182:185], v[198:201], v[110:113]
	v_mfma_f32_16x16x32_bf16 v[106:109], v[190:193], v[198:201], v[106:109]
	v_mfma_f32_16x16x32_bf16 v[78:81], v[182:185], v[206:209], v[78:81]
	v_mfma_f32_16x16x32_bf16 v[74:77], v[190:193], v[206:209], v[74:77]
	v_mfma_f32_16x16x32_bf16 v[50:53], v[182:185], v[214:217], v[50:53]
	v_mfma_f32_16x16x32_bf16 v[46:49], v[190:193], v[214:217], v[46:49]
	v_mfma_f32_16x16x32_bf16 v[22:25], v[182:185], v[224:227], v[22:25]
	v_mfma_f32_16x16x32_bf16 v[14:17], v[190:193], v[224:227], v[14:17]
	v_mfma_f32_16x16x32_bf16 v[110:113], v[186:189], v[202:205], v[110:113]
	v_mfma_f32_16x16x32_bf16 v[106:109], v[194:197], v[202:205], v[106:109]
	v_mfma_f32_16x16x32_bf16 v[78:81], v[186:189], v[210:213], v[78:81]
	v_mfma_f32_16x16x32_bf16 v[74:77], v[194:197], v[210:213], v[74:77]
	v_mfma_f32_16x16x32_bf16 v[50:53], v[186:189], v[218:221], v[50:53]
	v_mfma_f32_16x16x32_bf16 v[46:49], v[194:197], v[218:221], v[46:49]
	v_mfma_f32_16x16x32_bf16 v[22:25], v[186:189], v[228:231], v[22:25]
	v_mfma_f32_16x16x32_bf16 v[14:17], v[194:197], v[228:231], v[14:17]
	s_setprio 0
	s_add_i32 s58, s58, 2
	s_add_u32 s56, s56, 0x100
	s_addc_u32 s57, s57, 0
	s_add_u32 s16, s16, 0x100
	s_addc_u32 s17, s17, 0
	s_cmp_gt_u32 s58, 13
	s_barrier
	s_cbranch_scc0 .LBB0_2074
